# P4 P section: causal lane masks rebuilt with one v_cmp against a loop-invariant VGPR instead of two v_readlane spill reloads each
# speedup vs baseline: 1.0054x; 1.0044x over previous
.LBB0_609:
	s_or_b64 exec, exec, s[0:1]
	v_mov_b32_e32 v108, v0
	s_waitcnt lgkmcnt(0)
	v_mov_b32_e32 v1, s76
	v_mov_b32_e32 v2, s77
	s_barrier
	s_add_i32 s0, 0, 0x25d38
	v_readfirstlane_b32 s1, v2
	v_mov_b32_e32 v2, s78
	v_mov_b32_e32 v4, s74
	v_mov_b32_e32 v5, s75
	v_mov_b32_e32 v2, s0
	ds_read_b64 v[2:3], v2
	v_readfirstlane_b32 s46, v4
	v_readfirstlane_b32 s2, v1
	v_readfirstlane_b32 s39, v5
	s_mov_b32 s35, 0
	s_waitcnt lgkmcnt(0)
	v_readfirstlane_b32 s4, v2
	v_readfirstlane_b32 s5, v3
	s_cmpk_gt_i32 s46, 0xff
	v_writelane_b32 v243, s4, 14
	v_readfirstlane_b32 s3, v108
	s_nop 0
	v_writelane_b32 v243, s5, 15
	s_cbranch_scc1 .LBB0_825
	s_add_u32 s4, s2, 0x7400000
	s_addc_u32 s5, s1, 0
	s_add_u32 s40, s2, 0x17e00000
	s_addc_u32 s41, s1, 0
	s_add_u32 s0, s2, 0x300000
	v_writelane_b32 v243, s0, 16
	s_addc_u32 s0, s1, 0
	v_writelane_b32 v243, s0, 17
	s_add_u32 s0, s2, 0x1a200000
	v_writelane_b32 v243, s0, 19
	s_addc_u32 s0, s1, 0
	s_ashr_i32 s28, s3, 6
	v_writelane_b32 v243, s0, 20
	s_mul_i32 s0, s28, 0x2080
	s_add_i32 s0, s0, 0
	s_add_i32 s47, s0, 0x14f00
	s_lshl_b32 s0, s46, 3
	s_add_i32 s42, s28, s0
	s_lshl_b32 s33, s39, 3
	s_cmpk_eq_i32 s39, 0x100
	s_cselect_b64 s[8:9], -1, 0
	s_and_b64 s[6:7], s[8:9], exec
	s_movk_i32 s0, 0x330
	v_cmp_gt_i32_e64 s[6:7], s0, v108
	v_and_b32_e32 v1, 3, v108
	s_cselect_b32 s16, 0x4800, 0
	v_writelane_b32 v243, s6, 21
	s_cselect_b32 s18, 0xffffb800, 0
	s_lshl_b32 s17, s28, 4
	v_writelane_b32 v243, s7, 22
	v_cmp_eq_u32_e64 s[6:7], 0, v1
	v_ashrrev_i32_e32 v123, 2, v108
	s_movk_i32 s0, 0x70
	v_writelane_b32 v243, s6, 23
	s_cmp_gt_u32 s3, 63
	v_and_b32_e32 v111, 63, v108
	v_writelane_b32 v243, s7, 24
	s_movk_i32 s6, 0x8ff
	v_cmp_lt_i32_e64 s[6:7], s6, v108
	v_mul_lo_u32 v2, v123, s0
	v_add_u32_e32 v110, 0, v2
	v_writelane_b32 v243, s6, 25
	v_lshlrev_b32_e32 v2, 1, v111
	v_lshlrev_b32_e32 v112, 3, v1
	v_writelane_b32 v243, s7, 26
	s_cselect_b64 s[6:7], -1, 0
	s_cmp_lt_u32 s3, 64
	s_cselect_b64 s[10:11], -1, 0
	s_add_i32 s29, 0, 0x10700
	s_movk_i32 s3, 0xa0
	v_sub_u32_e32 v156, 0, v2
	v_mad_u64_u32 v[2:3], s[14:15], v123, s3, v[110:111]
	v_lshlrev_b32_e32 v118, 4, v1
	s_add_u32 s43, s2, 0x2ce00000
	v_and_b32_e32 v1, 7, v108
	v_bfe_u32 v158, v108, 3, 3
	s_addc_u32 s44, s1, 0
	v_mul_u32_u24_e32 v3, 0x410, v1
	v_lshlrev_b32_e32 v7, 2, v158
	s_add_i32 s1, 0, 0x8800
	v_add3_u32 v159, s47, v3, v7
	v_add_u32_e32 v3, s1, v112
	s_lshl_b32 s2, s28, 5
	s_mul_i32 s1, s39, 0x88
	s_add_i32 s2, s2, 0
	s_add_i32 s19, s42, s1
	v_bfe_u32 v113, v108, 4, 2
	s_cmp_lt_i32 s19, s16
	v_and_b32_e32 v117, 15, v108
	v_lshlrev_b32_e32 v122, 2, v113
	s_cselect_b64 s[14:15], -1, 0
	v_or_b32_e32 v151, s17, v117
	v_sub_u32_e32 v244, v151, v122
	v_subrev_u32_e32 v245, 64, v244
	v_or_b32_e32 v7, s17, v122
	s_and_b64 s[16:17], s[14:15], exec
	s_cselect_b32 s1, 0, s18
	s_add_i32 s3, s1, s19
	s_mul_hi_i32 s1, s3, 0x30c30c31
	s_and_b64 s[20:21], s[8:9], s[14:15]
	s_lshr_b32 s14, s1, 31
	s_ashr_i32 s1, s1, 10
	s_add_i32 s1, s1, s14
	v_writelane_b32 v243, s10, 27
	s_mul_i32 s14, s1, 0xffffeb00
	s_add_i32 s31, s14, s3
	v_writelane_b32 v243, s11, 28
	s_and_b64 s[14:15], s[20:21], exec
	v_writelane_b32 v243, s20, 29
	v_cmp_gt_i32_e64 s[50:51], v122, v151
	v_lshl_add_u32 v11, v7, 1, 0
	v_writelane_b32 v243, s21, 30
	v_writelane_b32 v243, s50, 31
	v_or_b32_e32 v7, 2, v122
	s_brev_b32 s3, 16
	v_writelane_b32 v243, s51, 32
	v_cmp_lt_i32_e64 s[50:51], v122, v151
	s_cselect_b32 s3, s3, 0xc600000
	s_lshl_b32 s14, s31, 1
	v_writelane_b32 v243, s50, 33
	s_add_i32 s14, s14, 0x7fffe400
	s_and_b32 s30, s14, 0x7fffffc0
	v_writelane_b32 v243, s51, 34
	v_cmp_gt_i32_e64 s[50:51], v7, v151
	v_or_b32_e32 v7, 3, v122
	s_lshl_b32 s14, s19, 5
	v_writelane_b32 v243, s50, 35
	s_and_b32 s34, s14, 0x3e0
	s_and_b64 s[14:15], s[20:21], exec
	v_writelane_b32 v243, s51, 36
	v_cmp_gt_i32_e64 s[50:51], v7, v151
	v_or_b32_e32 v7, 16, v122
	s_mov_b32 s16, 0x1000000
	v_writelane_b32 v243, s50, 37
	s_mul_hi_i32 s14, s31, 0x92492493
	s_cselect_b32 s36, s16, 0xb800000
	v_writelane_b32 v243, s51, 38
	v_cmp_gt_i32_e64 s[50:51], v7, v151
	v_or_b32_e32 v7, 17, v122
	s_add_i32 s14, s14, s31
	v_writelane_b32 v243, s50, 39
	s_lshr_b32 s15, s14, 31
	s_ashr_i32 s14, s14, 7
	v_writelane_b32 v243, s51, 40
	v_cmp_gt_i32_e64 s[50:51], v7, v151
	v_or_b32_e32 v7, 18, v122
	s_add_i32 s14, s14, s15
	v_writelane_b32 v243, s50, 41
	s_lshl_b32 s37, s14, 6
	s_mulk_i32 s14, 0xe0
	v_writelane_b32 v243, s51, 42
	v_cmp_gt_i32_e64 s[50:51], v7, v151
	v_or_b32_e32 v7, 19, v122
	s_sub_i32 s14, s31, s14
	v_writelane_b32 v243, s50, 43
	s_lshl_b32 s38, s14, 5
	s_cmp_gt_i32 s28, -1
	v_writelane_b32 v243, s51, 44
	v_cmp_gt_i32_e64 s[50:51], v7, v151
	v_or_b32_e32 v7, 32, v122
	s_cselect_b64 s[84:85], -1, 0
	v_writelane_b32 v243, s50, 45
	s_cmp_gt_i32 s28, 0
	s_cselect_b64 s[14:15], -1, 0
	v_writelane_b32 v243, s51, 46
	v_cmp_gt_i32_e64 s[50:51], v7, v151
	v_or_b32_e32 v7, 33, v122
	s_cmp_gt_i32 s28, 1
	v_writelane_b32 v243, s50, 47
	s_cselect_b64 s[16:17], -1, 0
	s_cmp_gt_i32 s28, 2
	v_writelane_b32 v243, s51, 48
	v_cmp_gt_i32_e64 s[50:51], v7, v151
	v_or_b32_e32 v7, 34, v122
	s_cselect_b64 s[18:19], -1, 0
	v_writelane_b32 v243, s50, 49
	s_cmp_gt_i32 s28, 3
	s_cselect_b64 s[20:21], -1, 0
	v_writelane_b32 v243, s51, 50
	v_cmp_gt_i32_e64 s[50:51], v7, v151
	v_or_b32_e32 v7, 35, v122
	s_cmp_gt_i32 s28, 4
	v_writelane_b32 v243, s50, 51
	s_cselect_b64 s[22:23], -1, 0
	s_cmp_gt_i32 s28, 5
	v_writelane_b32 v243, s51, 52
	v_cmp_gt_i32_e64 s[50:51], v7, v151
	v_or_b32_e32 v7, 48, v122
	v_bfe_u32 v5, v108, 2, 2
	v_writelane_b32 v243, s50, 53
	v_lshlrev_b32_e32 v116, 3, v113
	v_lshlrev_b32_e32 v6, 2, v111
	v_writelane_b32 v243, s51, 54
	v_cmp_gt_i32_e64 s[50:51], v7, v151
	v_or_b32_e32 v7, 49, v122
	s_cselect_b64 s[24:25], -1, 0
	v_writelane_b32 v243, s50, 55
	s_cmp_gt_i32 s28, 6
	v_add_u32_e32 v153, s29, v6
	v_writelane_b32 v243, s51, 56
	v_cmp_gt_i32_e64 s[50:51], v7, v151
	v_or_b32_e32 v7, 50, v122
	v_add_u32_e32 v155, 0, v6
	v_writelane_b32 v243, s50, 57
	v_and_b32_e32 v163, 28, v6
	v_or_b32_e32 v6, v116, v5
	v_writelane_b32 v243, s51, 58
	v_cmp_gt_i32_e64 s[50:51], v7, v151
	v_or_b32_e32 v7, 51, v122
	s_cselect_b64 s[26:27], -1, 0
	v_writelane_b32 v243, s50, 59
	s_cmpk_lt_i32 s31, 0xe00
	v_or_b32_e32 v5, v122, v5
	v_writelane_b32 v243, s51, 60
	v_cmp_gt_i32_e64 s[50:51], v7, v151
	v_or_b32_e32 v7, 64, v122
	v_mad_u32_u24 v164, v5, s0, v3
	v_writelane_b32 v243, s50, 61
	v_mul_u32_u24_e32 v5, 0x110, v6
	v_mad_u32_u24 v169, v6, s0, v3
	v_writelane_b32 v243, s51, 62
	v_cmp_gt_i32_e64 s[50:51], v7, v151
	v_or_b32_e32 v7, 0x41, v122
	s_movk_i32 s0, 0x400
	v_writelane_b32 v243, s50, 63
	s_cselect_b32 s3, s36, s3
	s_mov_b32 s31, 0xe00000
	v_writelane_b32 v242, s51, 0
	v_cmp_gt_i32_e64 s[50:51], v7, v151
	v_or_b32_e32 v7, 0x42, v122
	v_add3_u32 v168, s2, v112, v5
	v_writelane_b32 v242, s50, 1
	s_cselect_b32 s2, s0, 0xe00
	s_cselect_b32 s0, s37, s30
	v_writelane_b32 v242, s51, 2
	v_cmp_gt_i32_e64 s[50:51], v7, v151
	v_or_b32_e32 v7, 0x43, v122
	s_cselect_b32 s30, s38, s34
	v_writelane_b32 v242, s50, 3
	s_cselect_b32 s31, s31, 0x700000
	s_add_u32 s3, s43, s3
	v_writelane_b32 v242, s51, 4
	v_cmp_gt_i32_e64 s[50:51], v7, v151
	v_or_b32_e32 v7, 0x50, v122
	v_cmp_gt_i32_e64 s[56:57], v7, v151
	v_or_b32_e32 v7, 0x51, v122
	v_cmp_gt_i32_e64 s[58:59], v7, v151
	v_or_b32_e32 v7, 0x52, v122
	v_cmp_gt_i32_e64 s[60:61], v7, v151
	v_or_b32_e32 v7, 0x53, v122
	v_cmp_gt_i32_e64 s[62:63], v7, v151
	v_or_b32_e32 v7, 0x60, v122
	v_cmp_gt_i32_e64 s[64:65], v7, v151
	v_or_b32_e32 v7, 0x61, v122
	v_cmp_gt_i32_e64 s[66:67], v7, v151
	v_or_b32_e32 v7, 0x62, v122
	s_addc_u32 s34, s44, 0
	s_mul_hi_i32 s36, s31, s1
	s_mul_i32 s31, s31, s1
	v_cmp_gt_i32_e64 s[68:69], v7, v151
	v_or_b32_e32 v7, 0x63, v122
	s_add_u32 s3, s3, s31
	v_cmp_gt_i32_e64 s[70:71], v7, v151
	v_or_b32_e32 v7, 0x70, v122
	s_addc_u32 s31, s34, s36
	s_ashr_i32 s1, s0, 31
	v_cmp_gt_i32_e64 s[72:73], v7, v151
	v_or_b32_e32 v7, 0x71, v122
	s_lshl_b64 s[0:1], s[0:1], 1
	v_mov_b32_e32 v115, 0
	v_and_b32_e32 v114, 48, v108
	v_cmp_gt_i32_e64 s[74:75], v7, v151
	v_or_b32_e32 v7, 0x72, v122
	s_add_u32 s0, s3, s0
	v_lshlrev_b32_e32 v4, 3, v1
	v_or_b32_e32 v160, 8, v158
	v_lshl_add_u64 v[120:121], s[40:41], 0, v[114:115]
	v_add_u32_e32 v10, 0, v114
	v_cmp_gt_i32_e64 s[76:77], v7, v151
	v_or_b32_e32 v7, 0x73, v122
	s_addc_u32 s1, s31, s1
	v_lshlrev_b32_e32 v114, 4, v1
	v_or_b32_e32 v1, s30, v158
	v_or_b32_e32 v161, 16, v158
	v_cmp_gt_i32_e64 s[78:79], v7, v151
	v_lshl_add_u64 v[6:7], s[0:1], 0, v[114:115]
	v_mad_i64_i32 v[8:9], s[0:1], s2, v1, 0
	v_or_b32_e32 v1, s30, v160
	v_or_b32_e32 v162, 24, v158
	v_lshl_add_u64 v[124:125], v[8:9], 1, v[6:7]
	v_mad_i64_i32 v[8:9], s[0:1], s2, v1, 0
	v_or_b32_e32 v1, s30, v161
	v_writelane_b32 v242, s50, 5
	v_lshl_add_u64 v[126:127], v[8:9], 1, v[6:7]
	v_mad_i64_i32 v[8:9], s[0:1], s2, v1, 0
	v_or_b32_e32 v1, s30, v162
	v_writelane_b32 v242, s51, 6
	v_lshl_add_u64 v[128:129], v[8:9], 1, v[6:7]
	v_mad_i64_i32 v[8:9], s[0:1], s2, v1, 0
	v_max_i32_e32 v1, 0x700, v108
	v_writelane_b32 v242, s43, 7
	v_sub_u32_e32 v1, v1, v108
	v_writelane_b32 v242, s44, 9
	s_lshl_b32 s0, s42, 5
	v_add_u32_e32 v1, 0x1ff, v1
	v_lshlrev_b32_e32 v176, 2, v108
	v_lshl_add_u64 v[130:131], v[8:9], 1, v[6:7]
	v_writelane_b32 v242, s42, 10
	s_and_b32 s0, s0, 0x3e0
	v_add_u32_e32 v3, 0, v176
	v_lshlrev_b32_e32 v8, 2, v1
	v_writelane_b32 v242, s0, 11
	v_add_u32_e32 v3, 0x12b00, v3
	s_movk_i32 s0, 0xdff
	v_and_b32_e32 v8, 0xfffff800, v8
	v_lshrrev_b32_e32 v5, 9, v1
	v_cmp_lt_u32_e32 vcc, s0, v1
	v_cmp_gt_u32_e64 s[0:1], 2.0, v1
	v_add_u32_e32 v1, v3, v8
	v_add_u32_e32 v6, 1, v5
	v_add_u32_e32 v5, -1, v5
	v_cmp_ge_u32_e64 s[2:3], v1, v3
	s_and_b64 s[0:1], s[2:3], s[0:1]
	v_cmp_lt_u32_e64 s[2:3], 1, v5
	v_lshrrev_b32_e32 v7, 1, v5
	v_and_b32_e32 v5, 2, v5
	v_writelane_b32 v242, s2, 13
	v_and_b32_e32 v3, 0xfffffe, v6
	s_and_b64 s[0:1], vcc, s[0:1]
	v_writelane_b32 v242, s3, 14
	v_cmp_eq_u32_e64 s[2:3], 0, v5
	v_mov_b32_e32 v119, v115
	v_and_b32_e32 v12, 0x7f, v108
	v_writelane_b32 v242, s2, 15
	v_lshl_add_u32 v177, v3, 9, v108
	v_mul_u32_u24_e32 v13, 0x110, v117
	v_writelane_b32 v242, s3, 16
	v_cmp_ne_u32_e64 s[2:3], v6, v3
	v_lshl_add_u32 v3, v108, 4, 0
	v_or_b32_e32 v132, 0xffffff00, v12
	v_writelane_b32 v242, s2, 17
	v_add_u32_e32 v7, 1, v7
	v_add_u32_e32 v179, 0xc000, v3
	v_writelane_b32 v242, s3, 18
	v_writelane_b32 v242, s0, 19
	v_mbcnt_hi_u32_b32 v184, -1, v212
	v_bfrev_b32_e32 v6, 0.5
	v_writelane_b32 v242, s1, 20
	v_writelane_b32 v242, s40, 21
	s_lshl_b32 s1, s28, 1
	s_movk_i32 s49, 0x100
	v_writelane_b32 v242, s41, 22
	v_lshl_add_u64 v[134:135], s[40:41], 0, v[118:119]
	s_lshl_b32 s41, s39, 4
	v_writelane_b32 v242, s39, 23
	s_sub_i32 s0, 0, s41
	v_writelane_b32 v242, s0, 24
	s_lshl_b32 s0, s46, 4
	s_add_i32 s0, s0, s1
	s_add_i32 s0, s0, 0x7fffe400
	v_writelane_b32 v242, s0, 25
	s_add_i32 s0, 0, 0x25de0
	v_writelane_b32 v242, s0, 27
	s_add_i32 s0, 0, 0x25dd0
	v_writelane_b32 v242, s0, 29
	s_add_i32 s0, s47, 0x820
	v_writelane_b32 v242, s0, 30
	s_add_i32 s0, s47, 0xc30
	v_writelane_b32 v242, s0, 31
	s_add_i32 s0, s47, 0x1040
	v_writelane_b32 v242, s0, 33
	s_add_i32 s0, s47, 0x1450
	v_writelane_b32 v242, s0, 34
	s_add_i32 s0, s47, 0x1860
	v_writelane_b32 v242, s0, 35
	v_sub_u32_e32 v133, 0xff, v123
	v_sub_u32_e32 v152, 0xff, v151
	v_add_u32_e32 v154, 0x100, v153
	v_cmp_lt_u32_e64 s[10:11], 15, v111
	v_cmp_eq_u32_e64 s[12:13], 0, v111
	v_add_u32_e32 v157, 0xffffff00, v151
	v_add_u32_e32 v165, 0xe00, v164
	v_add_u32_e32 v166, 0x1c00, v164
	v_add_u32_e32 v167, 0x2a00, v164
	v_add_u32_e32 v170, 0x2200, v168
	v_add_u32_e32 v171, 0xe00, v169
	v_add_u32_e32 v172, 0x4400, v168
	v_add_u32_e32 v173, 0x1c00, v169
	v_add_u32_e32 v174, 0x6600, v168
	v_add_u32_e32 v175, 0x2a00, v169
	v_mov_b32_e32 v1, v132
	v_add_u32_e32 v109, 0x200, v108
	v_and_b32_e32 v178, -2, v7
	v_add_u32_e32 v119, 0xfffffe00, v108
	v_add_u32_e32 v180, s29, v176
	s_sub_i32 s40, 0, s33
	v_add_u32_e32 v181, 0x10900, v155
	v_sub_u32_e32 v182, 0, v123
	v_lshlrev_b32_e32 v136, 1, v116
	s_mov_b32 s42, 0x3f2aaaab
	v_mov_b32_e32 v183, 0x3ecc95a3
	s_mov_b32 s43, 0x3f317218
	s_mov_b32 s44, 0x7f800000
	s_mov_b32 s45, 0x33800000
	v_lshlrev_b32_e32 v138, 2, v122
	v_add_u32_e32 v185, v2, v118
	s_xor_b64 s[28:29], s[8:9], -1
	v_lshlrev_b32_e32 v114, 1, v4
	v_writelane_b32 v242, s47, 36
	s_add_i32 s0, s47, 0x1c70
	v_add_u32_e32 v186, v11, v13
	v_mov_b32_e32 v2, v115
	v_mov_b32_e32 v3, v115
	v_mov_b32_e32 v4, v115
	v_mov_b32_e32 v5, v115
	v_mov_b32_e32 v140, 0x3f317218
	v_mov_b32_e32 v187, 0x7f800000
	v_mov_b32_e32 v188, 0x7fc00000
	v_mov_b32_e32 v189, 0xff800000
	v_lshl_or_b32 v190, v184, 2, v6
	v_add_u32_e32 v191, v10, v13
	v_mov_b32_e32 v192, 0x7c
	v_writelane_b32 v242, s0, 38
	s_branch .LBB0_612

.LBB0_716:
	v_lshl_add_u32 v141, v151, 2, s83
	ds_read_b32 v143, v141 offset:62720
	v_lshl_add_u32 v196, v122, 2, s83
	s_mov_b64 s[38:39], -1
	s_and_b64 vcc, exec, s[84:85]
	s_cbranch_vccz .LBB0_733
	ds_read_b128 v[198:201], v196 offset:62208
	v_cmp_gt_i32_e64 s[38:39], 0, v244
	s_waitcnt lgkmcnt(0)
	v_sub_f32_e32 v70, v198, v143
	v_mul_f32_e32 v70, 0x3fb8aa3b, v70
	v_sub_f32_e32 v71, v199, v143
	v_exp_f32_e32 v70, v70
	v_mul_f32_e32 v71, 0x3fb8aa3b, v71
	v_exp_f32_e32 v71, v71
	v_sub_f32_e32 v76, v200, v143
	v_mul_f32_e32 v76, 0x3fb8aa3b, v76
	v_fma_mixlo_f16 v70, v104, v70, 0
	v_exp_f32_e32 v76, v76
	v_sub_f32_e32 v77, v201, v143
	v_cndmask_b32_e64 v70, v70, 0, s[38:39]
	v_readlane_b32 s38, v243, 33
	v_mul_f32_e32 v77, 0x3fb8aa3b, v77
	v_fma_mixlo_f16 v71, v105, v71, 0
	v_readlane_b32 s39, v243, 34
	v_exp_f32_e32 v77, v77
	s_nop 0
	v_cndmask_b32_e64 v71, 0, v71, s[38:39]
	v_pack_b32_f16 v70, v70, v71
	v_fma_mixlo_f16 v71, v106, v76, 0
	v_cmp_gt_i32_e64 s[38:39], 2, v244
	v_fma_mixlo_f16 v76, v107, v77, 0
	s_nop 0
	v_cndmask_b32_e64 v71, v71, 0, s[38:39]
	v_cmp_gt_i32_e64 s[38:39], 3, v244
	s_nop 1
	v_cndmask_b32_e64 v76, v76, 0, s[38:39]
	v_pack_b32_f16 v71, v71, v76
	s_cbranch_execz .LBB0_734

.LBB0_719:
	ds_read_b128 v[104:107], v196 offset:62272
	v_cmp_gt_i32_e64 s[38:39], 16, v244
	s_waitcnt lgkmcnt(0)
	v_sub_f32_e32 v76, v104, v143
	v_sub_f32_e32 v77, v105, v143
	v_mul_f32_e32 v76, 0x3fb8aa3b, v76
	v_mul_f32_e32 v77, 0x3fb8aa3b, v77
	v_exp_f32_e32 v76, v76
	v_exp_f32_e32 v77, v77
	v_sub_f32_e32 v82, v106, v143
	v_mul_f32_e32 v82, 0x3fb8aa3b, v82
	v_fma_mixlo_f16 v72, v72, v76, 0
	v_fma_mixlo_f16 v73, v73, v77, 0
	v_exp_f32_e32 v76, v82
	v_sub_f32_e32 v77, v107, v143
	v_cndmask_b32_e64 v72, v72, 0, s[38:39]
	v_mul_f32_e32 v77, 0x3fb8aa3b, v77
	v_cmp_gt_i32_e64 s[38:39], 17, v244
	v_exp_f32_e32 v77, v77
	s_nop 0
	v_cndmask_b32_e64 v73, v73, 0, s[38:39]
	v_pack_b32_f16 v72, v72, v73
	v_fma_mixlo_f16 v73, v74, v76, 0
	v_cmp_gt_i32_e64 s[38:39], 18, v244
	v_fma_mixlo_f16 v74, v75, v77, 0
	s_nop 0
	v_cndmask_b32_e64 v73, v73, 0, s[38:39]
	v_cmp_gt_i32_e64 s[38:39], 19, v244
	s_nop 1
	v_cndmask_b32_e64 v74, v74, 0, s[38:39]
	v_pack_b32_f16 v73, v73, v74
	s_cbranch_execz .LBB0_736

.LBB0_721:
	ds_read_b128 v[74:77], v196 offset:62336
	v_cmp_gt_i32_e64 s[38:39], 32, v244
	s_waitcnt lgkmcnt(0)
	v_sub_f32_e32 v74, v74, v143
	v_mul_f32_e32 v74, 0x3fb8aa3b, v74
	v_sub_f32_e32 v75, v75, v143
	v_exp_f32_e32 v74, v74
	v_mul_f32_e32 v75, 0x3fb8aa3b, v75
	v_exp_f32_e32 v75, v75
	v_sub_f32_e32 v76, v76, v143
	v_mul_f32_e32 v76, 0x3fb8aa3b, v76
	v_fma_mixlo_f16 v74, v100, v74, 0
	v_exp_f32_e32 v76, v76
	v_sub_f32_e32 v77, v77, v143
	v_cndmask_b32_e64 v74, v74, 0, s[38:39]
	v_mul_f32_e32 v77, 0x3fb8aa3b, v77
	v_fma_mixlo_f16 v75, v101, v75, 0
	v_cmp_gt_i32_e64 s[38:39], 33, v244
	v_exp_f32_e32 v77, v77
	s_nop 0
	v_cndmask_b32_e64 v75, v75, 0, s[38:39]
	v_pack_b32_f16 v74, v74, v75
	v_fma_mixlo_f16 v75, v102, v76, 0
	v_cmp_gt_i32_e64 s[38:39], 34, v244
	v_fma_mixlo_f16 v76, v103, v77, 0
	s_nop 0
	v_cndmask_b32_e64 v75, v75, 0, s[38:39]
	v_cmp_gt_i32_e64 s[38:39], 35, v244
	s_nop 1
	v_cndmask_b32_e64 v76, v76, 0, s[38:39]
	v_pack_b32_f16 v75, v75, v76
	s_cbranch_execz .LBB0_738

.LBB0_723:
	ds_read_b128 v[100:103], v196 offset:62400
	v_cmp_gt_i32_e64 s[0:1], 48, v244
	s_waitcnt lgkmcnt(0)
	v_sub_f32_e32 v76, v100, v143
	v_mul_f32_e32 v76, 0x3fb8aa3b, v76
	v_sub_f32_e32 v77, v101, v143
	v_exp_f32_e32 v76, v76
	v_mul_f32_e32 v77, 0x3fb8aa3b, v77
	v_exp_f32_e32 v77, v77
	v_sub_f32_e32 v82, v102, v143
	v_mul_f32_e32 v82, 0x3fb8aa3b, v82
	v_fma_mixlo_f16 v76, v92, v76, 0
	v_exp_f32_e32 v82, v82
	v_sub_f32_e32 v83, v103, v143
	v_cndmask_b32_e64 v76, v76, 0, s[0:1]
	v_mul_f32_e32 v83, 0x3fb8aa3b, v83
	v_fma_mixlo_f16 v77, v93, v77, 0
	v_cmp_gt_i32_e64 s[0:1], 49, v244
	v_exp_f32_e32 v83, v83
	s_nop 0
	v_cndmask_b32_e64 v77, v77, 0, s[0:1]
	v_pack_b32_f16 v76, v76, v77
	v_fma_mixlo_f16 v77, v94, v82, 0
	v_cmp_gt_i32_e64 s[0:1], 50, v244
	v_fma_mixlo_f16 v82, v95, v83, 0
	s_nop 0
	v_cndmask_b32_e64 v77, v77, 0, s[0:1]
	v_cmp_gt_i32_e64 s[0:1], 51, v244
	s_nop 1
	v_cndmask_b32_e64 v82, v82, 0, s[0:1]
	v_pack_b32_f16 v77, v77, v82
	s_cbranch_execz .LBB0_740

.LBB0_725:
	ds_read_b128 v[92:95], v196 offset:62464
	v_cmp_gt_i32_e64 s[0:1], 0, v245
	s_waitcnt lgkmcnt(0)
	v_sub_f32_e32 v82, v92, v143
	v_mul_f32_e32 v82, 0x3fb8aa3b, v82
	v_sub_f32_e32 v83, v93, v143
	v_exp_f32_e32 v82, v82
	v_mul_f32_e32 v83, 0x3fb8aa3b, v83
	v_exp_f32_e32 v83, v83
	v_sub_f32_e32 v92, v94, v143
	v_mul_f32_e32 v92, 0x3fb8aa3b, v92
	v_fma_mixlo_f16 v82, v96, v82, 0
	v_exp_f32_e32 v92, v92
	v_sub_f32_e32 v93, v95, v143
	v_cndmask_b32_e64 v82, v82, 0, s[0:1]
	v_mul_f32_e32 v93, 0x3fb8aa3b, v93
	v_fma_mixlo_f16 v83, v97, v83, 0
	v_cmp_gt_i32_e64 s[0:1], 1, v245
	v_exp_f32_e32 v93, v93
	s_nop 0
	v_cndmask_b32_e64 v83, v83, 0, s[0:1]
	v_pack_b32_f16 v82, v82, v83
	v_fma_mixlo_f16 v83, v98, v92, 0
	v_cmp_gt_i32_e64 s[0:1], 2, v245
	v_fma_mixlo_f16 v92, v99, v93, 0
	s_nop 0
	v_cndmask_b32_e64 v83, v83, 0, s[0:1]
	v_cmp_gt_i32_e64 s[0:1], 3, v245
	s_nop 1
	v_cndmask_b32_e64 v92, v92, 0, s[0:1]
	v_pack_b32_f16 v83, v83, v92
	s_cbranch_execz .LBB0_742

.LBB0_2009:
	s_add_i32 s3, 0, 0x25d38
	v_mov_b32_e32 v1, s3
	ds_read_b64 v[2:3], v1
	v_readfirstlane_b32 s3, v104
	s_cmpk_gt_i32 s54, 0xff
	s_waitcnt lgkmcnt(0)
	v_readfirstlane_b32 s4, v2
	v_readfirstlane_b32 s5, v3
	s_nop 0
	v_writelane_b32 v243, s4, 25
	s_nop 1
	v_writelane_b32 v243, s5, 26
	s_cbranch_scc1 .LBB0_2237
	s_or_b32 s42, s0, s33
	s_add_u32 s4, s2, 0x7400000
	s_addc_u32 s5, s1, 0
	s_add_u32 s36, s2, 0x17e00000
	s_addc_u32 s37, s1, 0
	s_add_u32 s0, s2, 0x300000
	v_writelane_b32 v242, s0, 41
	s_addc_u32 s0, s1, 0
	v_writelane_b32 v242, s0, 43
	s_add_u32 s0, s2, 0x1a200000
	v_writelane_b32 v243, s0, 29
	s_addc_u32 s0, s1, 0
	s_ashr_i32 s26, s3, 6
	v_writelane_b32 v242, s0, 25
	s_mul_i32 s0, s26, 0x2080
	s_add_i32 s43, s0, 0
	s_lshl_b32 s0, s54, 3
	s_add_i32 s15, s26, s0
	s_movk_i32 s0, 0x330
	v_cmp_gt_i32_e64 s[6:7], s0, v104
	v_readlane_b32 s14, v243, 23
	v_and_b32_e32 v1, 3, v104
	v_writelane_b32 v243, s6, 17
	s_add_i32 s43, s43, 0x14f00
	s_lshl_b32 s44, s14, 3
	v_writelane_b32 v243, s7, 18
	v_cmp_eq_u32_e64 s[6:7], 0, v1
	s_lshl_b32 s9, s26, 4
	s_cmp_gt_u32 s3, 63
	v_writelane_b32 v242, s6, 19
	v_and_b32_e32 v107, 63, v104
	v_ashrrev_i32_e32 v119, 2, v104
	v_writelane_b32 v242, s7, 20
	s_movk_i32 s6, 0x8ff
	v_cmp_lt_i32_e64 s[6:7], s6, v104
	s_movk_i32 s0, 0x70
	v_mul_lo_u32 v2, v119, s0
	v_writelane_b32 v242, s6, 13
	v_cmp_eq_u32_e64 s[12:13], 0, v107
	v_add_u32_e32 v106, 0, v2
	v_writelane_b32 v242, s7, 14
	s_cselect_b64 s[6:7], -1, 0
	s_cmp_lt_u32 s3, 64
	s_cselect_b64 s[10:11], -1, 0
	s_add_i32 s8, 0, 0x10700
	s_cmp_lg_u32 s42, 0
	v_lshlrev_b32_e32 v2, 1, v107
	v_writelane_b32 v243, s12, 31
	s_movk_i32 s3, 0xa0
	s_cselect_b64 s[84:85], -1, 0
	s_sub_i32 s45, 0, s33
	v_lshlrev_b32_e32 v108, 3, v1
	v_sub_u32_e32 v152, 0, v2
	v_writelane_b32 v243, s13, 32
	v_mad_u64_u32 v[2:3], s[12:13], v119, s3, v[106:107]
	v_lshlrev_b32_e32 v114, 4, v1
	s_add_u32 s38, s2, 0x2ce00000
	v_and_b32_e32 v1, 7, v104
	v_bfe_u32 v154, v104, 3, 3
	s_addc_u32 s39, s1, 0
	v_mul_u32_u24_e32 v3, 0x410, v1
	v_lshlrev_b32_e32 v7, 2, v154
	s_add_i32 s1, 0, 0x8800
	v_add3_u32 v155, s43, v3, v7
	v_add_u32_e32 v3, s1, v108
	s_lshl_b32 s2, s26, 5
	s_mul_i32 s1, s14, 0x88
	s_add_i32 s2, s2, 0
	s_add_i32 s1, s15, s1
	s_cmp_lt_i32 s1, s42
	s_cselect_b64 s[12:13], -1, 0
	s_cmp_ge_i32 s1, s33
	v_writelane_b32 v243, s15, 16
	s_cselect_b64 s[14:15], -1, 0
	s_and_b64 s[16:17], s[14:15], exec
	s_cselect_b32 s3, s45, s33
	s_add_i32 s18, s3, s1
	v_writelane_b32 v242, s10, 15
	s_mul_hi_i32 s1, s18, 0x30c30c31
	s_lshr_b32 s3, s1, 31
	v_writelane_b32 v242, s11, 16
	s_ashr_i32 s1, s1, 10
	v_readlane_b32 s16, v242, 27
	s_add_i32 s1, s1, s3
	v_readlane_b32 s17, v242, 28
	s_mul_i32 s3, s1, 0xffffeb00
	v_bfe_u32 v109, v104, 4, 2
	s_or_b64 s[14:15], s[16:17], s[14:15]
	s_add_i32 s35, s3, s18
	v_and_b32_e32 v113, 15, v104
	v_lshlrev_b32_e32 v118, 2, v109
	s_mov_b32 s3, 0xc600000
	s_and_b64 s[16:17], s[14:15], exec
	v_or_b32_e32 v147, s9, v113
	v_sub_u32_e32 v244, v147, v118
	v_subrev_u32_e32 v245, 64, v244
	v_or_b32_e32 v7, s9, v118
	s_cselect_b32 s3, s3, 0x8000000
	s_lshl_b32 s9, s35, 1
	s_add_i32 s9, s9, 0x7fffe400
	s_lshl_b32 s16, s18, 5
	s_and_b32 s9, s9, 0x7fffffc0
	s_and_b32 s28, s16, 0x3e0
	s_and_b64 s[14:15], s[14:15], exec
	s_mov_b32 s16, 0xb800000
	s_mul_hi_i32 s14, s35, 0x92492493
	s_cselect_b32 s29, s16, 0x1000000
	s_add_i32 s14, s14, s35
	s_lshr_b32 s15, s14, 31
	s_ashr_i32 s14, s14, 7
	s_add_i32 s14, s14, s15
	s_lshl_b32 s30, s14, 6
	s_mulk_i32 s14, 0xe0
	s_sub_i32 s14, s35, s14
	s_lshl_b32 s34, s14, 5
	s_cmp_gt_i32 s26, -1
	s_cselect_b64 s[82:83], -1, 0
	s_cmp_gt_i32 s26, 0
	s_cselect_b64 s[14:15], -1, 0
	s_cmp_gt_i32 s26, 1
	s_cselect_b64 s[16:17], -1, 0
	s_cmp_gt_i32 s26, 2
	s_cselect_b64 s[18:19], -1, 0
	s_cmp_gt_i32 s26, 3
	s_cselect_b64 s[20:21], -1, 0
	s_cmp_gt_i32 s26, 4
	s_cselect_b64 s[22:23], -1, 0
	s_cmp_gt_i32 s26, 5
	s_cselect_b64 s[24:25], -1, 0
	s_cmp_gt_i32 s26, 6
	s_cselect_b64 s[26:27], -1, 0
	s_and_b64 s[12:13], s[84:85], s[12:13]
	v_writelane_b32 v242, s12, 17
	v_lshl_add_u32 v11, v7, 1, 0
	v_or_b32_e32 v7, 2, v118
	v_writelane_b32 v242, s13, 18
	v_cmp_gt_i32_e64 s[12:13], v118, v147
	v_bfe_u32 v5, v104, 2, 2
	v_lshlrev_b32_e32 v112, 3, v109
	v_writelane_b32 v243, s12, 33
	v_lshlrev_b32_e32 v6, 2, v107
	v_add_u32_e32 v149, s8, v6
	v_writelane_b32 v243, s13, 34
	v_cmp_lt_i32_e64 s[12:13], v118, v147
	v_add_u32_e32 v151, 0, v6
	v_and_b32_e32 v159, 28, v6
	v_writelane_b32 v243, s12, 35
	v_or_b32_e32 v6, v112, v5
	s_cmpk_lt_i32 s35, 0xe00
	v_writelane_b32 v243, s13, 36
	v_cmp_gt_i32_e64 s[12:13], v7, v147
	v_or_b32_e32 v7, 3, v118
	v_or_b32_e32 v5, v118, v5
	v_writelane_b32 v243, s12, 37
	v_mad_u32_u24 v160, v5, s0, v3
	v_mul_u32_u24_e32 v5, 0x110, v6
	v_writelane_b32 v243, s13, 38
	v_cmp_gt_i32_e64 s[12:13], v7, v147
	v_or_b32_e32 v7, 16, v118
	v_mad_u32_u24 v165, v6, s0, v3
	v_writelane_b32 v243, s12, 39
	s_movk_i32 s0, 0x400
	s_cselect_b32 s3, s29, s3
	v_writelane_b32 v243, s13, 40
	v_cmp_gt_i32_e64 s[12:13], v7, v147
	v_or_b32_e32 v7, 17, v118
	v_add3_u32 v164, s2, v108, v5
	v_writelane_b32 v243, s12, 41
	s_cselect_b32 s2, s0, 0xe00
	s_cselect_b32 s0, s30, s9
	v_writelane_b32 v243, s13, 42
	v_cmp_gt_i32_e64 s[12:13], v7, v147
	v_or_b32_e32 v7, 18, v118
	s_cselect_b32 s9, s34, s28
	v_writelane_b32 v243, s12, 43
	v_mov_b32_e32 v111, 0
	v_and_b32_e32 v110, 48, v104
	v_writelane_b32 v243, s13, 44
	v_cmp_gt_i32_e64 s[12:13], v7, v147
	v_or_b32_e32 v7, 19, v118
	v_lshlrev_b32_e32 v4, 3, v1
	v_writelane_b32 v243, s12, 45
	v_or_b32_e32 v156, 8, v154
	v_lshl_add_u64 v[116:117], s[36:37], 0, v[110:111]
	v_writelane_b32 v243, s13, 46
	v_cmp_gt_i32_e64 s[12:13], v7, v147
	v_or_b32_e32 v7, 32, v118
	v_add_u32_e32 v10, 0, v110
	v_writelane_b32 v243, s12, 47
	v_lshlrev_b32_e32 v110, 4, v1
	v_or_b32_e32 v1, s9, v154
	v_writelane_b32 v243, s13, 48
	v_cmp_gt_i32_e64 s[12:13], v7, v147
	v_or_b32_e32 v7, 33, v118
	v_or_b32_e32 v157, 16, v154
	v_writelane_b32 v243, s12, 49
	v_or_b32_e32 v158, 24, v154
	v_lshlrev_b32_e32 v172, 2, v104
	v_writelane_b32 v243, s13, 50
	v_cmp_gt_i32_e64 s[12:13], v7, v147
	v_or_b32_e32 v7, 34, v118
	v_add_u32_e32 v3, 0, v172
	v_writelane_b32 v243, s12, 51
	v_add_u32_e32 v3, 0x12b00, v3
	v_and_b32_e32 v12, 0x7f, v104
	v_writelane_b32 v243, s13, 52
	v_cmp_gt_i32_e64 s[12:13], v7, v147
	v_or_b32_e32 v7, 35, v118
	v_mul_u32_u24_e32 v13, 0x110, v113
	v_writelane_b32 v243, s12, 53
	v_or_b32_e32 v128, 0xffffff00, v12
	v_mov_b32_e32 v115, v111
	v_writelane_b32 v243, s13, 54
	v_cmp_gt_i32_e64 s[12:13], v7, v147
	v_or_b32_e32 v7, 48, v118
	v_mbcnt_hi_u32_b32 v180, -1, v212
	v_writelane_b32 v243, s12, 55
	s_mov_b32 s31, 0
	v_sub_u32_e32 v129, 0xff, v119
	v_writelane_b32 v243, s13, 56
	v_cmp_gt_i32_e64 s[12:13], v7, v147
	v_or_b32_e32 v7, 49, v118
	v_sub_u32_e32 v148, 0xff, v147
	v_writelane_b32 v243, s12, 57
	s_movk_i32 s52, 0x100
	v_add_u32_e32 v150, 0x100, v149
	v_writelane_b32 v243, s13, 58
	v_cmp_gt_i32_e64 s[12:13], v7, v147
	v_or_b32_e32 v7, 50, v118
	v_cmp_lt_u32_e64 s[10:11], 15, v107
	v_writelane_b32 v243, s12, 59
	v_add_u32_e32 v153, 0xffffff00, v147
	v_add_u32_e32 v161, 0xe00, v160
	v_writelane_b32 v243, s13, 60
	v_cmp_gt_i32_e64 s[12:13], v7, v147
	v_or_b32_e32 v7, 51, v118
	v_add_u32_e32 v162, 0x1c00, v160
	v_writelane_b32 v243, s12, 61
	v_add_u32_e32 v163, 0x2a00, v160
	v_add_u32_e32 v166, 0x2200, v164
	v_writelane_b32 v243, s13, 62
	v_cmp_gt_i32_e64 s[12:13], v7, v147
	v_or_b32_e32 v7, 64, v118
	v_add_u32_e32 v167, 0xe00, v165
	v_writelane_b32 v243, s12, 63
	v_writelane_b32 v243, s36, 27
	v_add_u32_e32 v168, 0x4400, v164
	v_writelane_b32 v242, s13, 0
	v_cmp_gt_i32_e64 s[12:13], v7, v147
	v_or_b32_e32 v7, 0x41, v118
	v_writelane_b32 v243, s37, 28
	v_writelane_b32 v242, s12, 1
	v_add_u32_e32 v169, 0x1c00, v165
	v_add_u32_e32 v170, 0x6600, v164
	v_writelane_b32 v242, s13, 2
	v_cmp_gt_i32_e64 s[12:13], v7, v147
	v_or_b32_e32 v7, 0x42, v118
	v_add_u32_e32 v171, 0x2a00, v165
	v_writelane_b32 v242, s12, 3
	v_add_u32_e32 v105, 0x200, v104
	v_lshl_add_u64 v[130:131], s[36:37], 0, v[114:115]
	v_writelane_b32 v242, s13, 4
	v_cmp_gt_i32_e64 s[12:13], v7, v147
	v_or_b32_e32 v7, 0x43, v118
	v_add_u32_e32 v115, 0xfffffe00, v104
	v_writelane_b32 v242, s12, 5
	v_add_u32_e32 v176, s8, v172
	v_add_u32_e32 v177, 0x10900, v151
	v_writelane_b32 v242, s13, 6
	v_cmp_gt_i32_e64 s[12:13], v7, v147
	v_or_b32_e32 v7, 0x50, v118
	v_sub_u32_e32 v178, 0, v119
	v_writelane_b32 v242, s12, 11
	v_lshlrev_b32_e32 v132, 1, v112
	s_mov_b32 s47, 0x3f2aaaab
	v_writelane_b32 v242, s13, 12
	v_cmp_gt_i32_e64 s[12:13], v7, v147
	v_or_b32_e32 v7, 0x51, v118
	v_mov_b32_e32 v179, 0x3ecc95a3
	v_writelane_b32 v242, s12, 36
	s_mov_b32 s48, 0x3f317218
	s_mov_b32 s49, 0x7f800000
	v_writelane_b32 v242, s13, 37
	v_cmp_gt_i32_e64 s[12:13], v7, v147
	v_or_b32_e32 v7, 0x52, v118
	v_cmp_gt_i32_e64 s[60:61], v7, v147
	v_writelane_b32 v242, s12, 7
	v_or_b32_e32 v7, 0x53, v118
	v_cmp_gt_i32_e64 s[62:63], v7, v147
	v_writelane_b32 v242, s13, 8
	v_or_b32_e32 v7, 0x60, v118
	s_mov_b32 s12, 0xe00000
	v_cmp_gt_i32_e64 s[64:65], v7, v147
	v_or_b32_e32 v7, 0x61, v118
	s_cselect_b32 s12, s12, 0x700000
	s_add_u32 s3, s38, s3
	v_cmp_gt_i32_e64 s[66:67], v7, v147
	v_or_b32_e32 v7, 0x62, v118
	s_addc_u32 s13, s39, 0
	s_mul_hi_i32 s28, s12, s1
	s_mul_i32 s12, s12, s1
	v_cmp_gt_i32_e64 s[68:69], v7, v147
	v_or_b32_e32 v7, 0x63, v118
	s_add_u32 s3, s3, s12
	v_cmp_gt_i32_e64 s[70:71], v7, v147
	v_or_b32_e32 v7, 0x70, v118
	s_addc_u32 s12, s13, s28
	s_ashr_i32 s1, s0, 31
	v_cmp_gt_i32_e64 s[72:73], v7, v147
	v_or_b32_e32 v7, 0x71, v118
	s_lshl_b64 s[0:1], s[0:1], 1
	v_cmp_gt_i32_e64 s[74:75], v7, v147
	v_or_b32_e32 v7, 0x72, v118
	s_add_u32 s0, s3, s0
	v_cmp_gt_i32_e64 s[76:77], v7, v147
	v_or_b32_e32 v7, 0x73, v118
	s_addc_u32 s1, s12, s1
	v_cmp_gt_i32_e64 s[78:79], v7, v147
	v_lshl_add_u64 v[6:7], s[0:1], 0, v[110:111]
	v_mad_i64_i32 v[8:9], s[0:1], s2, v1, 0
	v_or_b32_e32 v1, s9, v156
	v_lshl_add_u64 v[120:121], v[8:9], 1, v[6:7]
	v_mad_i64_i32 v[8:9], s[0:1], s2, v1, 0
	v_or_b32_e32 v1, s9, v157
	v_lshl_add_u64 v[122:123], v[8:9], 1, v[6:7]
	v_mad_i64_i32 v[8:9], s[0:1], s2, v1, 0
	v_or_b32_e32 v1, s9, v158
	v_lshl_add_u64 v[124:125], v[8:9], 1, v[6:7]
	v_mad_i64_i32 v[8:9], s[0:1], s2, v1, 0
	v_max_i32_e32 v1, 0x700, v104
	v_sub_u32_e32 v1, v1, v104
	v_add_u32_e32 v1, 0x1ff, v1
	v_lshl_add_u64 v[126:127], v[8:9], 1, v[6:7]
	v_lshlrev_b32_e32 v8, 2, v1
	s_movk_i32 s0, 0xdff
	v_and_b32_e32 v8, 0xfffff800, v8
	v_lshrrev_b32_e32 v5, 9, v1
	v_cmp_lt_u32_e32 vcc, s0, v1
	v_cmp_gt_u32_e64 s[0:1], 2.0, v1
	v_add_u32_e32 v1, v3, v8
	v_writelane_b32 v242, s38, 29
	v_add_u32_e32 v6, 1, v5
	v_add_u32_e32 v5, -1, v5
	v_cmp_ge_u32_e64 s[2:3], v1, v3
	v_writelane_b32 v242, s39, 39
	s_and_b64 s[0:1], s[2:3], s[0:1]
	v_cmp_lt_u32_e64 s[2:3], 1, v5
	v_lshrrev_b32_e32 v7, 1, v5
	v_and_b32_e32 v5, 2, v5
	v_writelane_b32 v242, s2, 45
	v_and_b32_e32 v3, 0xfffffe, v6
	s_and_b64 s[0:1], vcc, s[0:1]
	v_writelane_b32 v242, s3, 46
	v_cmp_eq_u32_e64 s[2:3], 0, v5
	v_lshl_add_u32 v173, v3, 9, v104
	v_add_u32_e32 v7, 1, v7
	v_writelane_b32 v242, s2, 47
	v_mov_b32_e32 v1, v128
	v_and_b32_e32 v174, -2, v7
	v_writelane_b32 v242, s3, 48
	v_cmp_ne_u32_e64 s[2:3], v6, v3
	v_lshl_add_u32 v3, v104, 4, 0
	v_add_u32_e32 v175, 0xc000, v3
	v_writelane_b32 v242, s2, 49
	v_bfrev_b32_e32 v6, 0.5
	s_sub_i32 s46, 0, s44
	v_writelane_b32 v242, s3, 50
	v_writelane_b32 v242, s0, 51
	s_mov_b32 s50, 0x33800000
	v_lshlrev_b32_e32 v134, 2, v118
	v_writelane_b32 v242, s1, 52
	s_add_i32 s0, 0, 0x25de0
	v_writelane_b32 v243, s0, 14
	s_add_i32 s0, 0, 0x25db8
	v_writelane_b32 v242, s0, 23
	s_add_i32 s0, 0, 0x25dd0
	v_writelane_b32 v242, s0, 21
	s_add_i32 s0, 0, 0x25da8
	v_writelane_b32 v243, s0, 19
	s_add_i32 s0, 0, 0x25dd8
	v_writelane_b32 v243, s0, 20
	s_add_i32 s0, 0, 0x25db0
	v_writelane_b32 v242, s0, 10
	s_add_i32 s0, s43, 0x820
	v_writelane_b32 v242, s0, 31
	s_add_i32 s0, s43, 0xc30
	v_writelane_b32 v242, s0, 33
	s_add_i32 s0, s43, 0x1040
	v_writelane_b32 v242, s0, 34
	s_add_i32 s0, s43, 0x1450
	v_writelane_b32 v242, s0, 35
	s_add_i32 s0, s43, 0x1860
	v_add_u32_e32 v181, v2, v114
	s_xor_b64 s[28:29], s[84:85], -1
	v_lshlrev_b32_e32 v110, 1, v4
	v_writelane_b32 v242, s0, 38
	s_add_i32 s0, s43, 0x1c70
	v_add_u32_e32 v182, v11, v13
	v_mov_b32_e32 v2, v111
	v_mov_b32_e32 v3, v111
	v_mov_b32_e32 v4, v111
	v_mov_b32_e32 v5, v111
	v_mov_b32_e32 v136, 0x3f317218
	v_mov_b32_e32 v183, 0x7f800000
	v_mov_b32_e32 v184, 0x7fc00000
	v_mov_b32_e32 v185, 0xff800000
	v_lshl_or_b32 v186, v180, 2, v6
	v_add_u32_e32 v187, v10, v13
	v_mov_b32_e32 v188, 0x7c
	v_writelane_b32 v242, s0, 24
	s_branch .LBB0_2012

.LBB0_2116:
	v_lshl_add_u32 v137, v147, 2, s9
	ds_read_b32 v139, v137 offset:62720
	v_lshl_add_u32 v192, v118, 2, s9
	s_mov_b64 s[38:39], -1
	s_and_b64 vcc, exec, s[82:83]
	s_cbranch_vccz .LBB0_2133
	ds_read_b128 v[194:197], v192 offset:62208
	v_cmp_gt_i32_e64 s[12:13], 0, v244
	s_waitcnt lgkmcnt(0)
	v_sub_f32_e32 v70, v194, v139
	v_sub_f32_e32 v71, v195, v139
	v_mul_f32_e32 v70, 0x3fb8aa3b, v70
	v_mul_f32_e32 v71, 0x3fb8aa3b, v71
	v_exp_f32_e32 v70, v70
	v_exp_f32_e32 v71, v71
	v_sub_f32_e32 v193, v196, v139
	v_mul_f32_e32 v193, 0x3fb8aa3b, v193
	v_fma_mixlo_f16 v70, v100, v70, 0
	v_fma_mixlo_f16 v71, v101, v71, 0
	v_exp_f32_e32 v100, v193
	v_sub_f32_e32 v101, v197, v139
	v_cndmask_b32_e64 v70, v70, 0, s[12:13]
	v_readlane_b32 s12, v243, 35
	v_mul_f32_e32 v101, 0x3fb8aa3b, v101
	v_readlane_b32 s13, v243, 36
	v_exp_f32_e32 v101, v101
	s_nop 0
	v_cndmask_b32_e64 v71, 0, v71, s[12:13]
	v_pack_b32_f16 v70, v70, v71
	v_fma_mixlo_f16 v71, v102, v100, 0
	v_cmp_gt_i32_e64 s[12:13], 2, v244
	v_fma_mixlo_f16 v100, v103, v101, 0
	s_nop 0
	v_cndmask_b32_e64 v71, v71, 0, s[12:13]
	v_cmp_gt_i32_e64 s[12:13], 3, v244
	s_nop 1
	v_cndmask_b32_e64 v100, v100, 0, s[12:13]
	v_pack_b32_f16 v71, v71, v100
	s_cbranch_execz .LBB0_2134

.LBB0_2119:
	ds_read_b128 v[100:103], v192 offset:62272
	v_cmp_gt_i32_e64 s[12:13], 16, v244
	s_waitcnt lgkmcnt(0)
	v_sub_f32_e32 v100, v100, v139
	v_sub_f32_e32 v101, v101, v139
	v_mul_f32_e32 v100, 0x3fb8aa3b, v100
	v_mul_f32_e32 v101, 0x3fb8aa3b, v101
	v_exp_f32_e32 v100, v100
	v_exp_f32_e32 v101, v101
	v_sub_f32_e32 v102, v102, v139
	v_mul_f32_e32 v102, 0x3fb8aa3b, v102
	v_fma_mixlo_f16 v72, v72, v100, 0
	v_fma_mixlo_f16 v73, v73, v101, 0
	v_exp_f32_e32 v100, v102
	v_sub_f32_e32 v101, v103, v139
	v_cndmask_b32_e64 v72, v72, 0, s[12:13]
	v_mul_f32_e32 v101, 0x3fb8aa3b, v101
	v_cmp_gt_i32_e64 s[12:13], 17, v244
	v_exp_f32_e32 v101, v101
	s_nop 0
	v_cndmask_b32_e64 v73, v73, 0, s[12:13]
	v_pack_b32_f16 v72, v72, v73
	v_fma_mixlo_f16 v73, v74, v100, 0
	v_cmp_gt_i32_e64 s[12:13], 18, v244
	v_fma_mixlo_f16 v74, v75, v101, 0
	s_nop 0
	v_cndmask_b32_e64 v73, v73, 0, s[12:13]
	v_cmp_gt_i32_e64 s[12:13], 19, v244
	s_nop 1
	v_cndmask_b32_e64 v74, v74, 0, s[12:13]
	v_pack_b32_f16 v73, v73, v74
	s_cbranch_execz .LBB0_2136

.LBB0_2121:
	ds_read_b128 v[100:103], v192 offset:62336
	v_cmp_gt_i32_e64 s[12:13], 32, v244
	s_waitcnt lgkmcnt(0)
	v_sub_f32_e32 v74, v100, v139
	v_sub_f32_e32 v75, v101, v139
	v_mul_f32_e32 v74, 0x3fb8aa3b, v74
	v_mul_f32_e32 v75, 0x3fb8aa3b, v75
	v_exp_f32_e32 v74, v74
	v_exp_f32_e32 v75, v75
	v_sub_f32_e32 v100, v102, v139
	v_mul_f32_e32 v100, 0x3fb8aa3b, v100
	v_fma_mixlo_f16 v74, v96, v74, 0
	v_fma_mixlo_f16 v75, v97, v75, 0
	v_exp_f32_e32 v96, v100
	v_sub_f32_e32 v97, v103, v139
	v_cndmask_b32_e64 v74, v74, 0, s[12:13]
	v_mul_f32_e32 v97, 0x3fb8aa3b, v97
	v_cmp_gt_i32_e64 s[12:13], 33, v244
	v_exp_f32_e32 v97, v97
	s_nop 0
	v_cndmask_b32_e64 v75, v75, 0, s[12:13]
	v_pack_b32_f16 v74, v74, v75
	v_fma_mixlo_f16 v75, v98, v96, 0
	v_cmp_gt_i32_e64 s[12:13], 34, v244
	v_fma_mixlo_f16 v96, v99, v97, 0
	s_nop 0
	v_cndmask_b32_e64 v75, v75, 0, s[12:13]
	v_cmp_gt_i32_e64 s[12:13], 35, v244
	s_nop 1
	v_cndmask_b32_e64 v96, v96, 0, s[12:13]
	v_pack_b32_f16 v75, v75, v96
	s_cbranch_execz .LBB0_2138

.LBB0_2123:
	ds_read_b128 v[96:99], v192 offset:62400
	v_cmp_gt_i32_e64 s[0:1], 48, v244
	s_waitcnt lgkmcnt(0)
	v_sub_f32_e32 v96, v96, v139
	v_sub_f32_e32 v97, v97, v139
	v_mul_f32_e32 v96, 0x3fb8aa3b, v96
	v_mul_f32_e32 v97, 0x3fb8aa3b, v97
	v_exp_f32_e32 v96, v96
	v_exp_f32_e32 v97, v97
	v_sub_f32_e32 v98, v98, v139
	v_mul_f32_e32 v98, 0x3fb8aa3b, v98
	v_fma_mixlo_f16 v76, v76, v96, 0
	v_fma_mixlo_f16 v77, v77, v97, 0
	v_exp_f32_e32 v96, v98
	v_sub_f32_e32 v97, v99, v139
	v_cndmask_b32_e64 v76, v76, 0, s[0:1]
	v_mul_f32_e32 v97, 0x3fb8aa3b, v97
	v_cmp_gt_i32_e64 s[0:1], 49, v244
	v_exp_f32_e32 v97, v97
	s_nop 0
	v_cndmask_b32_e64 v77, v77, 0, s[0:1]
	v_pack_b32_f16 v76, v76, v77
	v_fma_mixlo_f16 v77, v78, v96, 0
	v_cmp_gt_i32_e64 s[0:1], 50, v244
	v_fma_mixlo_f16 v78, v79, v97, 0
	s_nop 0
	v_cndmask_b32_e64 v77, v77, 0, s[0:1]
	v_cmp_gt_i32_e64 s[0:1], 51, v244
	s_nop 1
	v_cndmask_b32_e64 v78, v78, 0, s[0:1]
	v_pack_b32_f16 v77, v77, v78
	s_cbranch_execz .LBB0_2140

.LBB0_2125:
	ds_read_b128 v[96:99], v192 offset:62464
	v_cmp_gt_i32_e64 s[0:1], 0, v245
	s_waitcnt lgkmcnt(0)
	v_sub_f32_e32 v78, v96, v139
	v_sub_f32_e32 v79, v97, v139
	v_mul_f32_e32 v78, 0x3fb8aa3b, v78
	v_mul_f32_e32 v79, 0x3fb8aa3b, v79
	v_exp_f32_e32 v78, v78
	v_exp_f32_e32 v79, v79
	v_sub_f32_e32 v96, v98, v139
	v_mul_f32_e32 v96, 0x3fb8aa3b, v96
	v_fma_mixlo_f16 v78, v92, v78, 0
	v_fma_mixlo_f16 v79, v93, v79, 0
	v_exp_f32_e32 v92, v96
	v_sub_f32_e32 v93, v99, v139
	v_cndmask_b32_e64 v78, v78, 0, s[0:1]
	v_mul_f32_e32 v93, 0x3fb8aa3b, v93
	v_cmp_gt_i32_e64 s[0:1], 1, v245
	v_exp_f32_e32 v93, v93
	s_nop 0
	v_cndmask_b32_e64 v79, v79, 0, s[0:1]
	v_pack_b32_f16 v78, v78, v79
	v_fma_mixlo_f16 v79, v94, v92, 0
	v_cmp_gt_i32_e64 s[0:1], 2, v245
	v_fma_mixlo_f16 v92, v95, v93, 0
	s_nop 0
	v_cndmask_b32_e64 v79, v79, 0, s[0:1]
	v_cmp_gt_i32_e64 s[0:1], 3, v245
	s_nop 1
	v_cndmask_b32_e64 v92, v92, 0, s[0:1]
	v_pack_b32_f16 v79, v79, v92
	s_cbranch_execz .LBB0_2142

.LBB0_2127:
	ds_read_b128 v[92:95], v192 offset:62528
	v_cmp_gt_i32_e64 s[0:1], 16, v245
	s_waitcnt lgkmcnt(0)
	v_sub_f32_e32 v93, v93, v139
	v_mul_f32_e32 v93, 0x3fb8aa3b, v93
	v_sub_f32_e32 v92, v92, v139
	v_exp_f32_e32 v93, v93
	v_mul_f32_e32 v92, 0x3fb8aa3b, v92
	v_exp_f32_e32 v92, v92
	v_sub_f32_e32 v94, v94, v139
	v_fma_mixlo_f16 v81, v81, v93, 0
	v_sub_f32_e32 v93, v95, v139
	v_mul_f32_e32 v94, 0x3fb8aa3b, v94
	v_mul_f32_e32 v93, 0x3fb8aa3b, v93
	v_fma_mixlo_f16 v80, v80, v92, 0
	v_exp_f32_e32 v92, v94
	v_exp_f32_e32 v93, v93
	v_cndmask_b32_e64 v80, v80, 0, s[0:1]
	v_cmp_gt_i32_e64 s[0:1], 17, v245
	s_nop 1
	v_cndmask_b32_e64 v81, v81, 0, s[0:1]
	v_pack_b32_f16 v80, v80, v81
	v_fma_mixlo_f16 v81, v82, v92, 0
	v_fma_mixlo_f16 v82, v83, v93, 0
	v_cndmask_b32_e64 v81, v81, 0, s[60:61]
	v_cndmask_b32_e64 v82, v82, 0, s[62:63]
	v_pack_b32_f16 v81, v81, v82
	s_cbranch_execz .LBB0_2144

.LBB0_3626:
	s_or_b64 exec, exec, s[0:1]
	s_load_dwordx2 s[0:1], s[80:81], 0xf0
	v_mov_b32_e32 v104, v0
	s_waitcnt lgkmcnt(0)
	s_barrier
	v_mov_b32_e32 v1, s0
	v_mov_b32_e32 v2, s1
	s_add_i32 s0, 0, 0x25d38
	v_readfirstlane_b32 s2, v2
	v_mov_b32_e32 v2, s79
	v_mov_b32_e32 v4, s77
	v_mov_b32_e32 v5, s78
	v_mov_b32_e32 v2, s0
	ds_read_b64 v[2:3], v2
	v_readfirstlane_b32 s52, v4
	v_readfirstlane_b32 s3, v1
	v_readfirstlane_b32 s53, v5
	s_mov_b32 s35, 0
	s_waitcnt lgkmcnt(0)
	v_readfirstlane_b32 s0, v2
	v_readfirstlane_b32 s1, v3
	s_cmpk_gt_i32 s52, 0xff
	v_writelane_b32 v243, s0, 27
	v_readfirstlane_b32 s10, v104
	s_nop 0
	v_writelane_b32 v243, s1, 28
	s_cbranch_scc1 .LBB0_3854
	s_add_u32 s4, s3, 0x7400000
	s_addc_u32 s5, s2, 0
	s_add_u32 s44, s3, 0x17e00000
	s_addc_u32 s45, s2, 0
	s_add_u32 s0, s3, 0x300000
	v_writelane_b32 v242, s0, 45
	s_addc_u32 s0, s2, 0
	v_writelane_b32 v242, s0, 47
	s_add_u32 s0, s3, 0x1a200000
	v_writelane_b32 v243, s0, 16
	s_addc_u32 s0, s2, 0
	s_ashr_i32 s28, s10, 6
	v_writelane_b32 v243, s0, 17
	s_mul_i32 s0, s28, 0x2080
	s_add_i32 s0, s0, 0
	s_add_i32 s48, s0, 0x14f00
	s_lshl_b32 s0, s52, 3
	s_add_i32 s46, s28, s0
	s_lshl_b32 s33, s53, 3
	s_cmpk_eq_i32 s53, 0x100
	s_cselect_b64 s[8:9], -1, 0
	s_and_b64 s[0:1], s[8:9], exec
	s_movk_i32 s1, 0x330
	v_cmp_gt_i32_e64 s[6:7], s1, v104
	v_and_b32_e32 v1, 3, v104
	s_cselect_b32 s16, 0x4800, 0
	v_writelane_b32 v242, s6, 13
	s_cselect_b32 s0, 3, 0
	s_lshl_b32 s17, s28, 4
	v_writelane_b32 v242, s7, 14
	v_cmp_eq_u32_e64 s[6:7], 0, v1
	v_ashrrev_i32_e32 v119, 2, v104
	s_movk_i32 s1, 0x70
	v_writelane_b32 v242, s6, 15
	s_cmp_gt_u32 s10, 63
	v_and_b32_e32 v107, 63, v104
	v_writelane_b32 v242, s7, 16
	s_movk_i32 s6, 0x8ff
	v_cmp_lt_i32_e64 s[6:7], s6, v104
	v_mul_lo_u32 v2, v119, s1
	v_add_u32_e32 v106, 0, v2
	v_writelane_b32 v242, s6, 17
	v_lshlrev_b32_e32 v2, 1, v107
	s_movk_i32 s14, 0xa0
	v_writelane_b32 v242, s7, 18
	s_cselect_b64 s[6:7], -1, 0
	s_cmp_lt_u32 s10, 64
	s_cselect_b64 s[10:11], -1, 0
	s_add_i32 s29, 0, 0x10700
	v_lshlrev_b32_e32 v108, 3, v1
	v_sub_u32_e32 v152, 0, v2
	v_mad_u64_u32 v[2:3], s[14:15], v119, s14, v[106:107]
	v_lshlrev_b32_e32 v114, 4, v1
	s_add_u32 s47, s3, 0x2ce00000
	v_and_b32_e32 v1, 7, v104
	v_bfe_u32 v154, v104, 3, 3
	s_addc_u32 s50, s2, 0
	v_mul_u32_u24_e32 v3, 0x410, v1
	v_lshlrev_b32_e32 v6, 2, v154
	s_add_i32 s2, 0, 0x8800
	v_add3_u32 v155, s48, v3, v6
	v_add_u32_e32 v3, s2, v108
	s_lshl_b32 s3, s28, 5
	s_mul_i32 s2, s53, 0x88
	s_add_i32 s3, s3, 0
	s_add_i32 s20, s46, s2
	s_cmp_lt_i32 s20, s16
	v_bfe_u32 v109, v104, 4, 2
	s_cselect_b64 s[42:43], -1, 0
	s_cmp_ge_i32 s20, s16
	v_and_b32_e32 v113, 15, v104
	v_lshlrev_b32_e32 v118, 2, v109
	s_cselect_b64 s[14:15], -1, 0
	v_or_b32_e32 v147, s17, v113
	v_sub_u32_e32 v244, v147, v118
	v_subrev_u32_e32 v245, 64, v244
	v_or_b32_e32 v8, s17, v118
	s_and_b64 s[16:17], s[8:9], s[14:15]
	s_and_b64 s[16:17], s[16:17], exec
	s_cselect_b32 s2, 0xffffb800, 0
	s_add_i32 s21, s2, s20
	s_bfe_i32 s2, s0, 0x10000
	s_and_b32 s16, s0, 1
	v_writelane_b32 v242, s10, 41
	s_bitcmp1_b32 s0, 0
	s_cselect_b64 s[18:19], -1, 0
	v_writelane_b32 v242, s11, 42
	s_cmp_eq_u32 s16, 0
	v_writelane_b32 v242, s18, 31
	s_cselect_b64 s[16:17], -1, 0
	s_mul_hi_i32 s22, s21, 0x30c30c31
	v_writelane_b32 v242, s19, 32
	s_and_b64 s[18:19], s[16:17], exec
	s_mov_b32 s23, 0xc600000
	s_mov_b32 s18, 0xb800000
	s_cselect_b32 s34, s23, 0x8000000
	s_cselect_b32 s54, s18, 0x1000000
	s_or_b64 s[14:15], s[16:17], s[14:15]
	s_lshr_b32 s16, s22, 31
	s_ashr_i32 s30, s22, 10
	s_add_i32 s30, s30, s16
	s_mul_i32 s16, s30, 0xffffeb00
	s_add_i32 s41, s16, s21
	s_and_b64 s[16:17], s[14:15], exec
	s_cselect_b32 s31, s23, 0x8000000
	s_lshl_b32 s16, s41, 1
	s_add_i32 s16, s16, 0x7fffe400
	s_and_b32 s36, s16, 0x7fffffc0
	s_lshl_b32 s16, s20, 5
	s_and_b32 s37, s16, 0x3e0
	s_mul_hi_i32 s19, s41, 0x92492493
	s_and_b64 s[14:15], s[14:15], exec
	s_cselect_b32 s38, s18, 0x1000000
	s_add_i32 s19, s19, s41
	s_lshr_b32 s14, s19, 31
	s_ashr_i32 s15, s19, 7
	s_add_i32 s14, s15, s14
	s_mul_i32 s15, s14, 0xe0
	s_lshl_b32 s39, s14, 6
	s_sub_i32 s14, s41, s15
	s_lshl_b32 s40, s14, 5
	s_cmp_gt_i32 s28, -1
	s_cselect_b64 s[84:85], -1, 0
	s_cmp_gt_i32 s28, 0
	s_cselect_b64 s[14:15], -1, 0
	s_cmp_gt_i32 s28, 1
	s_cselect_b64 s[16:17], -1, 0
	s_cmp_gt_i32 s28, 2
	s_cselect_b64 s[18:19], -1, 0
	s_cmp_gt_i32 s28, 3
	s_cselect_b64 s[20:21], -1, 0
	s_cmp_gt_i32 s28, 4
	s_cselect_b64 s[22:23], -1, 0
	s_cmp_gt_i32 s28, 5
	s_cselect_b64 s[24:25], -1, 0
	s_cmp_gt_i32 s28, 6
	s_cselect_b64 s[26:27], -1, 0
	s_and_b64 s[42:43], s[8:9], s[42:43]
	v_writelane_b32 v242, s42, 43
	v_lshl_add_u32 v12, v8, 1, 0
	v_or_b32_e32 v8, 2, v118
	v_writelane_b32 v242, s43, 44
	v_cmp_gt_i32_e64 s[42:43], v118, v147
	v_bfe_u32 v5, v104, 2, 2
	v_lshlrev_b32_e32 v112, 3, v109
	v_writelane_b32 v243, s42, 31
	v_lshlrev_b32_e32 v7, 2, v107
	v_add_u32_e32 v149, s29, v7
	v_writelane_b32 v243, s43, 32
	v_cmp_lt_i32_e64 s[42:43], v118, v147
	v_add_u32_e32 v151, 0, v7
	v_and_b32_e32 v159, 28, v7
	v_writelane_b32 v243, s42, 33
	v_or_b32_e32 v7, v112, v5
	v_or_b32_e32 v5, v118, v5
	v_writelane_b32 v243, s43, 34
	v_cmp_gt_i32_e64 s[42:43], v8, v147
	v_or_b32_e32 v8, 3, v118
	s_cmpk_lt_i32 s41, 0xe00
	v_writelane_b32 v243, s42, 35
	v_mad_u32_u24 v160, v5, s1, v3
	v_mul_u32_u24_e32 v5, 0x110, v7
	v_writelane_b32 v243, s43, 36
	v_cmp_gt_i32_e64 s[42:43], v8, v147
	v_or_b32_e32 v8, 16, v118
	v_add3_u32 v164, s3, v108, v5
	v_writelane_b32 v243, s42, 37
	s_cselect_b32 s3, s40, s37
	s_mov_b32 s37, 0xe00000
	v_writelane_b32 v243, s43, 38
	v_cmp_gt_i32_e64 s[42:43], v8, v147
	v_or_b32_e32 v8, 17, v118
	v_mad_u32_u24 v165, v7, s1, v3
	v_writelane_b32 v243, s42, 39
	s_movk_i32 s1, 0x400
	s_cselect_b32 s31, s38, s31
	v_writelane_b32 v243, s43, 40
	v_cmp_gt_i32_e64 s[42:43], v8, v147
	v_or_b32_e32 v8, 18, v118
	s_cselect_b32 s37, s37, 0x700000
	v_writelane_b32 v243, s42, 41
	s_cselect_b32 s1, s1, 0xe00
	s_cselect_b32 s36, s39, s36
	v_writelane_b32 v243, s43, 42
	v_cmp_gt_i32_e64 s[42:43], v8, v147
	v_or_b32_e32 v8, 19, v118
	s_mul_hi_i32 s38, s37, s30
	v_writelane_b32 v243, s42, 43
	s_mul_i32 s37, s37, s30
	s_add_u32 s30, s47, s31
	v_writelane_b32 v243, s43, 44
	v_cmp_gt_i32_e64 s[42:43], v8, v147
	v_or_b32_e32 v8, 32, v118
	s_addc_u32 s31, s50, 0
	v_writelane_b32 v243, s42, 45
	s_add_u32 s39, s30, s37
	s_addc_u32 s38, s31, s38
	v_writelane_b32 v243, s43, 46
	v_cmp_gt_i32_e64 s[42:43], v8, v147
	v_or_b32_e32 v8, 33, v118
	s_ashr_i32 s37, s36, 31
	v_writelane_b32 v243, s42, 47
	s_lshl_b64 s[30:31], s[36:37], 1
	v_mov_b32_e32 v111, 0
	v_writelane_b32 v243, s43, 48
	v_cmp_gt_i32_e64 s[42:43], v8, v147
	v_or_b32_e32 v8, 34, v118
	v_and_b32_e32 v110, 48, v104
	v_writelane_b32 v243, s42, 49
	s_add_u32 s30, s39, s30
	v_lshlrev_b32_e32 v4, 3, v1
	v_writelane_b32 v243, s43, 50
	v_cmp_gt_i32_e64 s[42:43], v8, v147
	v_or_b32_e32 v8, 35, v118
	v_or_b32_e32 v156, 8, v154
	v_writelane_b32 v243, s42, 51
	v_lshl_add_u64 v[116:117], s[44:45], 0, v[110:111]
	v_add_u32_e32 v6, 0, v110
	v_writelane_b32 v243, s43, 52
	v_cmp_gt_i32_e64 s[42:43], v8, v147
	v_or_b32_e32 v8, 48, v118
	s_addc_u32 s31, s38, s31
	v_writelane_b32 v243, s42, 53
	v_lshlrev_b32_e32 v110, 4, v1
	v_or_b32_e32 v1, s3, v154
	v_writelane_b32 v243, s43, 54
	v_cmp_gt_i32_e64 s[42:43], v8, v147
	v_or_b32_e32 v8, 49, v118
	v_or_b32_e32 v157, 16, v154
	v_writelane_b32 v243, s42, 55
	v_or_b32_e32 v158, 24, v154
	s_lshr_b32 s0, s0, 1
	v_writelane_b32 v243, s43, 56
	v_cmp_gt_i32_e64 s[42:43], v8, v147
	v_or_b32_e32 v8, 50, v118
	v_lshlrev_b32_e32 v172, 2, v104
	v_writelane_b32 v243, s42, 57
	v_add_u32_e32 v3, 0, v172
	v_add_u32_e32 v3, 0x12b00, v3
	v_writelane_b32 v243, s43, 58
	v_cmp_gt_i32_e64 s[42:43], v8, v147
	v_or_b32_e32 v8, 51, v118
	v_and_b32_e32 v13, 0x7f, v104
	v_writelane_b32 v243, s42, 59
	v_mul_u32_u24_e32 v14, 0x110, v113
	v_or_b32_e32 v128, 0xffffff00, v13
	v_writelane_b32 v243, s43, 60
	v_cmp_gt_i32_e64 s[42:43], v8, v147
	v_or_b32_e32 v8, 64, v118
	v_mov_b32_e32 v115, v111
	v_writelane_b32 v243, s42, 61
	v_mbcnt_hi_u32_b32 v180, -1, v212
	s_movk_i32 s49, 0x100
	v_writelane_b32 v243, s43, 62
	v_cmp_gt_i32_e64 s[42:43], v8, v147
	v_or_b32_e32 v8, 0x41, v118
	v_sub_u32_e32 v129, 0xff, v119
	v_writelane_b32 v243, s42, 63
	v_writelane_b32 v243, s34, 14
	s_mov_b32 s55, s35
	v_writelane_b32 v242, s43, 0
	v_cmp_gt_i32_e64 s[42:43], v8, v147
	v_or_b32_e32 v8, 0x42, v118
	v_writelane_b32 v243, s35, 15
	v_writelane_b32 v242, s42, 1
	v_sub_u32_e32 v148, 0xff, v147
	v_add_u32_e32 v150, 0x100, v149
	v_writelane_b32 v242, s43, 2
	v_cmp_gt_i32_e64 s[42:43], v8, v147
	v_or_b32_e32 v8, 0x43, v118
	v_cmp_lt_u32_e64 s[10:11], 15, v107
	v_writelane_b32 v242, s42, 3
	v_cmp_eq_u32_e64 s[12:13], 0, v107
	v_add_u32_e32 v153, 0xffffff00, v147
	v_writelane_b32 v242, s43, 4
	v_cmp_gt_i32_e64 s[42:43], v8, v147
	v_or_b32_e32 v8, 0x50, v118
	v_add_u32_e32 v161, 0xe00, v160
	v_writelane_b32 v242, s42, 5
	v_add_u32_e32 v162, 0x1c00, v160
	v_add_u32_e32 v163, 0x2a00, v160
	v_writelane_b32 v242, s43, 6
	v_cmp_gt_i32_e64 s[42:43], v8, v147
	v_or_b32_e32 v8, 0x51, v118
	v_cmp_gt_i32_e64 s[58:59], v8, v147
	v_or_b32_e32 v8, 0x52, v118
	v_cmp_gt_i32_e64 s[60:61], v8, v147
	v_or_b32_e32 v8, 0x53, v118
	v_cmp_gt_i32_e64 s[62:63], v8, v147
	v_or_b32_e32 v8, 0x60, v118
	v_cmp_gt_i32_e64 s[64:65], v8, v147
	v_or_b32_e32 v8, 0x61, v118
	v_cmp_gt_i32_e64 s[66:67], v8, v147
	v_or_b32_e32 v8, 0x62, v118
	v_cmp_gt_i32_e64 s[68:69], v8, v147
	v_or_b32_e32 v8, 0x63, v118
	v_cmp_gt_i32_e64 s[70:71], v8, v147
	v_or_b32_e32 v8, 0x70, v118
	v_cmp_gt_i32_e64 s[72:73], v8, v147
	v_or_b32_e32 v8, 0x71, v118
	v_cmp_gt_i32_e64 s[74:75], v8, v147
	v_or_b32_e32 v8, 0x72, v118
	v_cmp_gt_i32_e64 s[76:77], v8, v147
	v_or_b32_e32 v8, 0x73, v118
	v_writelane_b32 v242, s42, 11
	v_cmp_gt_i32_e64 s[78:79], v8, v147
	v_lshl_add_u64 v[8:9], s[30:31], 0, v[110:111]
	v_mad_i64_i32 v[10:11], s[30:31], s1, v1, 0
	v_or_b32_e32 v1, s3, v156
	v_writelane_b32 v242, s43, 12
	v_lshl_add_u64 v[120:121], v[10:11], 1, v[8:9]
	v_mad_i64_i32 v[10:11], s[30:31], s1, v1, 0
	v_or_b32_e32 v1, s3, v157
	v_writelane_b32 v242, s47, 9
	v_lshl_add_u64 v[122:123], v[10:11], 1, v[8:9]
	v_mad_i64_i32 v[10:11], s[30:31], s1, v1, 0
	v_or_b32_e32 v1, s3, v158
	v_writelane_b32 v242, s50, 30
	v_lshl_add_u64 v[124:125], v[10:11], 1, v[8:9]
	v_mad_i64_i32 v[10:11], s[30:31], s1, v1, 0
	s_lshl_b32 s1, s46, 5
	v_writelane_b32 v242, s46, 19
	s_and_b32 s1, s1, 0x3e0
	v_max_i32_e32 v1, 0x700, v104
	v_writelane_b32 v242, s1, 36
	v_sub_u32_e32 v1, v1, v104
	v_writelane_b32 v242, s54, 39
	s_and_b32 s1, s2, 3
	v_add_u32_e32 v1, 0x1ff, v1
	v_lshl_add_u64 v[126:127], v[10:11], 1, v[8:9]
	v_writelane_b32 v242, s55, 40
	s_lshl_b32 s0, s0, s1
	v_lshlrev_b32_e32 v9, 2, v1
	v_writelane_b32 v242, s0, 33
	s_movk_i32 s0, 0xdff
	v_and_b32_e32 v9, 0xfffff800, v9
	v_lshrrev_b32_e32 v5, 9, v1
	v_cmp_lt_u32_e32 vcc, s0, v1
	v_cmp_gt_u32_e64 s[0:1], 2.0, v1
	v_add_u32_e32 v1, v3, v9
	v_add_u32_e32 v7, 1, v5
	v_add_u32_e32 v5, -1, v5
	v_cmp_ge_u32_e64 s[2:3], v1, v3
	s_and_b64 s[0:1], s[2:3], s[0:1]
	v_cmp_lt_u32_e64 s[2:3], 1, v5
	v_lshrrev_b32_e32 v8, 1, v5
	v_and_b32_e32 v5, 2, v5
	v_writelane_b32 v242, s2, 53
	v_and_b32_e32 v3, 0xfffffe, v7
	s_and_b64 s[0:1], vcc, s[0:1]
	v_writelane_b32 v242, s3, 54
	v_cmp_eq_u32_e64 s[2:3], 0, v5
	s_lshl_b32 s43, s53, 4
	v_lshl_add_u32 v173, v3, 9, v104
	v_writelane_b32 v242, s2, 55
	v_add_u32_e32 v8, 1, v8
	v_add_u32_e32 v166, 0x2200, v164
	v_writelane_b32 v242, s3, 56
	v_cmp_ne_u32_e64 s[2:3], v7, v3
	v_lshl_add_u32 v3, v104, 4, 0
	v_add_u32_e32 v175, 0xc000, v3
	v_writelane_b32 v242, s2, 57
	v_bfrev_b32_e32 v7, 0.5
	v_add_u32_e32 v167, 0xe00, v165
	v_writelane_b32 v242, s3, 58
	v_writelane_b32 v242, s0, 49
	v_add_u32_e32 v168, 0x4400, v164
	v_add_u32_e32 v169, 0x1c00, v165
	v_writelane_b32 v242, s1, 50
	v_writelane_b32 v242, s44, 25
	s_sub_i32 s0, 0, s43
	s_lshl_b32 s1, s28, 1
	v_writelane_b32 v242, s45, 26
	v_writelane_b32 v242, s0, 23
	s_lshl_b32 s0, s52, 4
	s_add_i32 s0, s0, s1
	s_add_i32 s0, s0, 0x7fffe400
	v_writelane_b32 v242, s0, 51
	s_add_i32 s0, 0, 0x25de0
	v_writelane_b32 v242, s0, 21
	s_add_i32 s0, 0, 0x25db8
	v_writelane_b32 v243, s0, 19
	s_add_i32 s0, 0, 0x25dd0
	v_writelane_b32 v243, s0, 20
	s_add_i32 s0, 0, 0x25da8
	v_writelane_b32 v242, s0, 10
	s_add_i32 s0, 0, 0x25dd8
	v_writelane_b32 v243, s0, 21
	s_add_i32 s0, 0, 0x25db0
	v_writelane_b32 v243, s0, 23
	s_add_i32 s0, s48, 0x820
	v_writelane_b32 v242, s0, 34
	s_add_i32 s0, s48, 0xc30
	v_writelane_b32 v242, s0, 35
	s_add_i32 s0, s48, 0x1040
	v_writelane_b32 v242, s0, 38
	s_add_i32 s0, s48, 0x1450
	v_writelane_b32 v242, s0, 24
	s_add_i32 s0, s48, 0x1860
	v_writelane_b32 v242, s0, 27
	v_add_u32_e32 v170, 0x6600, v164
	v_add_u32_e32 v171, 0x2a00, v165
	v_mov_b32_e32 v1, v128
	v_add_u32_e32 v105, 0x200, v104
	v_and_b32_e32 v174, -2, v8
	v_lshl_add_u64 v[130:131], s[44:45], 0, v[114:115]
	v_add_u32_e32 v115, 0xfffffe00, v104
	v_add_u32_e32 v176, s29, v172
	s_sub_i32 s42, 0, s33
	v_add_u32_e32 v177, 0x10900, v151
	v_sub_u32_e32 v178, 0, v119
	s_movk_i32 s55, 0x3000
	v_lshlrev_b32_e32 v132, 1, v112
	s_mov_b32 s44, 0x3f2aaaab
	v_mov_b32_e32 v179, 0x3ecc95a3
	s_mov_b32 s45, 0x3f317218
	s_mov_b32 s46, 0x7f800000
	s_mov_b32 s47, 0x33800000
	v_lshlrev_b32_e32 v134, 2, v118
	v_add_u32_e32 v181, v2, v114
	s_xor_b64 s[28:29], s[8:9], -1
	v_lshlrev_b32_e32 v110, 1, v4
	v_writelane_b32 v242, s48, 7
	s_add_i32 s0, s48, 0x1c70
	v_add_u32_e32 v182, v12, v14
	v_mov_b32_e32 v2, v111
	v_mov_b32_e32 v3, v111
	v_mov_b32_e32 v4, v111
	v_mov_b32_e32 v5, v111
	v_mov_b32_e32 v136, 0x3f317218
	v_mov_b32_e32 v183, 0x7f800000
	v_mov_b32_e32 v184, 0x7fc00000
	v_mov_b32_e32 v185, 0xff800000
	v_lshl_or_b32 v186, v180, 2, v7
	v_add_u32_e32 v187, v6, v14
	v_mov_b32_e32 v188, 0x7c
	v_writelane_b32 v242, s0, 29
	v_writelane_b32 v243, s53, 29
	s_branch .LBB0_3629

.LBB0_3733:
	v_lshl_add_u32 v137, v147, 2, s83
	ds_read_b32 v139, v137 offset:62720
	v_lshl_add_u32 v192, v118, 2, s83
	s_mov_b64 s[38:39], -1
	s_and_b64 vcc, exec, s[84:85]
	s_cbranch_vccz .LBB0_3750
	ds_read_b128 v[194:197], v192 offset:62208
	v_cmp_gt_i32_e64 s[38:39], 0, v244
	s_waitcnt lgkmcnt(0)
	v_sub_f32_e32 v70, v194, v139
	v_sub_f32_e32 v71, v195, v139
	v_mul_f32_e32 v70, 0x3fb8aa3b, v70
	v_mul_f32_e32 v71, 0x3fb8aa3b, v71
	v_exp_f32_e32 v70, v70
	v_exp_f32_e32 v71, v71
	v_sub_f32_e32 v193, v196, v139
	v_mul_f32_e32 v193, 0x3fb8aa3b, v193
	v_fma_mixlo_f16 v70, v100, v70, 0
	v_fma_mixlo_f16 v71, v101, v71, 0
	v_exp_f32_e32 v100, v193
	v_sub_f32_e32 v101, v197, v139
	v_cndmask_b32_e64 v70, v70, 0, s[38:39]
	v_readlane_b32 s38, v243, 33
	v_mul_f32_e32 v101, 0x3fb8aa3b, v101
	v_readlane_b32 s39, v243, 34
	v_exp_f32_e32 v101, v101
	s_nop 0
	v_cndmask_b32_e64 v71, 0, v71, s[38:39]
	v_pack_b32_f16 v70, v70, v71
	v_fma_mixlo_f16 v71, v102, v100, 0
	v_cmp_gt_i32_e64 s[38:39], 2, v244
	v_fma_mixlo_f16 v100, v103, v101, 0
	s_nop 0
	v_cndmask_b32_e64 v71, v71, 0, s[38:39]
	v_cmp_gt_i32_e64 s[38:39], 3, v244
	s_nop 1
	v_cndmask_b32_e64 v100, v100, 0, s[38:39]
	v_pack_b32_f16 v71, v71, v100
	s_cbranch_execz .LBB0_3751

.LBB0_3736:
	ds_read_b128 v[100:103], v192 offset:62272
	v_cmp_gt_i32_e64 s[0:1], 16, v244
	s_waitcnt lgkmcnt(0)
	v_sub_f32_e32 v100, v100, v139
	v_sub_f32_e32 v101, v101, v139
	v_mul_f32_e32 v100, 0x3fb8aa3b, v100
	v_mul_f32_e32 v101, 0x3fb8aa3b, v101
	v_exp_f32_e32 v100, v100
	v_exp_f32_e32 v101, v101
	v_sub_f32_e32 v102, v102, v139
	v_mul_f32_e32 v102, 0x3fb8aa3b, v102
	v_fma_mixlo_f16 v72, v72, v100, 0
	v_fma_mixlo_f16 v73, v73, v101, 0
	v_exp_f32_e32 v100, v102
	v_sub_f32_e32 v101, v103, v139
	v_cndmask_b32_e64 v72, v72, 0, s[0:1]
	v_mul_f32_e32 v101, 0x3fb8aa3b, v101
	v_cmp_gt_i32_e64 s[0:1], 17, v244
	v_exp_f32_e32 v101, v101
	s_nop 0
	v_cndmask_b32_e64 v73, v73, 0, s[0:1]
	v_pack_b32_f16 v72, v72, v73
	v_fma_mixlo_f16 v73, v74, v100, 0
	v_cmp_gt_i32_e64 s[0:1], 18, v244
	v_fma_mixlo_f16 v74, v75, v101, 0
	s_nop 0
	v_cndmask_b32_e64 v73, v73, 0, s[0:1]
	v_cmp_gt_i32_e64 s[0:1], 19, v244
	s_nop 1
	v_cndmask_b32_e64 v74, v74, 0, s[0:1]
	v_pack_b32_f16 v73, v73, v74
	s_cbranch_execz .LBB0_3753

.LBB0_3738:
	ds_read_b128 v[100:103], v192 offset:62336
	v_cmp_gt_i32_e64 s[0:1], 32, v244
	s_waitcnt lgkmcnt(0)
	v_sub_f32_e32 v74, v100, v139
	v_sub_f32_e32 v75, v101, v139
	v_mul_f32_e32 v74, 0x3fb8aa3b, v74
	v_mul_f32_e32 v75, 0x3fb8aa3b, v75
	v_exp_f32_e32 v74, v74
	v_exp_f32_e32 v75, v75
	v_sub_f32_e32 v100, v102, v139
	v_mul_f32_e32 v100, 0x3fb8aa3b, v100
	v_fma_mixlo_f16 v74, v96, v74, 0
	v_fma_mixlo_f16 v75, v97, v75, 0
	v_exp_f32_e32 v96, v100
	v_sub_f32_e32 v97, v103, v139
	v_cndmask_b32_e64 v74, v74, 0, s[0:1]
	v_mul_f32_e32 v97, 0x3fb8aa3b, v97
	v_cmp_gt_i32_e64 s[0:1], 33, v244
	v_exp_f32_e32 v97, v97
	s_nop 0
	v_cndmask_b32_e64 v75, v75, 0, s[0:1]
	v_pack_b32_f16 v74, v74, v75
	v_fma_mixlo_f16 v75, v98, v96, 0
	v_cmp_gt_i32_e64 s[0:1], 34, v244
	v_fma_mixlo_f16 v96, v99, v97, 0
	s_nop 0
	v_cndmask_b32_e64 v75, v75, 0, s[0:1]
	v_cmp_gt_i32_e64 s[0:1], 35, v244
	s_nop 1
	v_cndmask_b32_e64 v96, v96, 0, s[0:1]
	v_pack_b32_f16 v75, v75, v96
	s_cbranch_execz .LBB0_3755

.LBB0_3744:
	ds_read_b128 v[92:95], v192 offset:62528
	v_cmp_gt_i32_e64 s[0:1], 16, v245
	s_waitcnt lgkmcnt(0)
	v_sub_f32_e32 v93, v93, v139
	v_mul_f32_e32 v93, 0x3fb8aa3b, v93
	v_sub_f32_e32 v92, v92, v139
	v_exp_f32_e32 v93, v93
	v_mul_f32_e32 v92, 0x3fb8aa3b, v92
	v_exp_f32_e32 v92, v92
	v_sub_f32_e32 v94, v94, v139
	v_fma_mixlo_f16 v81, v81, v93, 0
	v_sub_f32_e32 v93, v95, v139
	v_mul_f32_e32 v94, 0x3fb8aa3b, v94
	v_mul_f32_e32 v93, 0x3fb8aa3b, v93
	v_fma_mixlo_f16 v80, v80, v92, 0
	v_exp_f32_e32 v92, v94
	v_exp_f32_e32 v93, v93
	v_cndmask_b32_e64 v80, v80, 0, s[0:1]
	v_cndmask_b32_e64 v81, v81, 0, s[58:59]
	v_pack_b32_f16 v80, v80, v81
	v_fma_mixlo_f16 v81, v82, v92, 0
	v_fma_mixlo_f16 v82, v83, v93, 0
	v_cndmask_b32_e64 v81, v81, 0, s[60:61]
	v_cndmask_b32_e64 v82, v82, 0, s[62:63]
	v_pack_b32_f16 v81, v81, v82
	s_cbranch_execz .LBB0_3761

.LBB0_4989:
	s_or_b64 exec, exec, s[0:1]
	v_readlane_b32 s0, v243, 8
	v_readlane_b32 s1, v243, 9
	v_mov_b32_e32 v104, v0
	s_waitcnt lgkmcnt(0)
	v_mov_b32_e32 v1, s0
	v_mov_b32_e32 v2, s1
	s_barrier
	s_add_i32 s0, 0, 0x25d38
	v_readfirstlane_b32 s12, v2
	v_mov_b32_e32 v2, s79
	v_mov_b32_e32 v4, s77
	v_mov_b32_e32 v5, s78
	v_mov_b32_e32 v2, s0
	ds_read_b64 v[2:3], v2
	v_readfirstlane_b32 s50, v4
	v_readfirstlane_b32 s13, v1
	v_readfirstlane_b32 s44, v5
	s_mov_b32 s31, 0
	s_waitcnt lgkmcnt(0)
	v_readfirstlane_b32 s0, v2
	v_readfirstlane_b32 s1, v3
	s_cmpk_gt_i32 s50, 0xff
	v_writelane_b32 v243, s0, 27
	v_readfirstlane_b32 s8, v104
	s_nop 0
	v_writelane_b32 v243, s1, 28
	s_cbranch_scc1 .LBB0_5217
	s_add_u32 s0, s13, 0x7400000
	s_addc_u32 s1, s12, 0
	s_add_u32 s46, s13, 0x17e00000
	s_addc_u32 s47, s12, 0
	s_add_u32 s2, s13, 0x300000
	v_writelane_b32 v243, s80, 12
	v_writelane_b32 v242, s2, 45
	s_addc_u32 s2, s12, 0
	v_writelane_b32 v243, s81, 13
	v_writelane_b32 v242, s2, 47
	s_add_u32 s2, s13, 0x1a200000
	v_writelane_b32 v243, s2, 16
	s_addc_u32 s2, s12, 0
	s_ashr_i32 s26, s8, 6
	v_writelane_b32 v243, s2, 17
	s_mul_i32 s2, s26, 0x2080
	s_add_i32 s2, s2, 0
	s_add_i32 s48, s2, 0x14f00
	s_lshl_b32 s2, s50, 3
	s_add_i32 s45, s26, s2
	s_lshl_b32 s33, s44, 3
	s_cmpk_eq_i32 s44, 0x100
	s_cselect_b64 s[6:7], -1, 0
	s_and_b64 s[2:3], s[6:7], exec
	s_movk_i32 s3, 0x330
	v_cmp_gt_i32_e64 s[4:5], s3, v104
	v_and_b32_e32 v1, 3, v104
	s_cselect_b32 s16, 0x4800, 0
	v_writelane_b32 v242, s4, 13
	s_cselect_b32 s2, 3, 0
	s_lshl_b32 s17, s26, 4
	v_writelane_b32 v242, s5, 14
	v_cmp_eq_u32_e64 s[4:5], 0, v1
	v_ashrrev_i32_e32 v119, 2, v104
	s_movk_i32 s3, 0x70
	v_writelane_b32 v242, s4, 15
	s_cmp_gt_u32 s8, 63
	v_and_b32_e32 v107, 63, v104
	v_writelane_b32 v242, s5, 16
	s_movk_i32 s4, 0x8ff
	v_cmp_lt_i32_e64 s[4:5], s4, v104
	v_mul_lo_u32 v2, v119, s3
	v_add_u32_e32 v106, 0, v2
	v_writelane_b32 v242, s4, 17
	v_lshlrev_b32_e32 v2, 1, v107
	s_movk_i32 s14, 0xa0
	v_writelane_b32 v242, s5, 18
	s_cselect_b64 s[4:5], -1, 0
	s_cmp_lt_u32 s8, 64
	s_cselect_b64 s[8:9], -1, 0
	s_add_i32 s27, 0, 0x10700
	s_sub_i32 s18, 0, s16
	v_lshlrev_b32_e32 v108, 3, v1
	v_sub_u32_e32 v152, 0, v2
	v_mad_u64_u32 v[2:3], s[14:15], v119, s14, v[106:107]
	v_lshlrev_b32_e32 v114, 4, v1
	s_add_u32 s51, s13, 0x2ce00000
	v_and_b32_e32 v1, 7, v104
	v_bfe_u32 v154, v104, 3, 3
	s_addc_u32 s52, s12, 0
	v_mul_u32_u24_e32 v3, 0x410, v1
	v_lshlrev_b32_e32 v6, 2, v154
	s_add_i32 s12, 0, 0x8800
	v_add3_u32 v155, s48, v3, v6
	v_add_u32_e32 v3, s12, v108
	s_lshl_b32 s29, s26, 5
	s_mul_i32 s12, s44, 0x88
	s_add_i32 s29, s29, 0
	s_add_i32 s19, s45, s12
	s_cmp_lt_i32 s19, s16
	s_cselect_b64 s[42:43], -1, 0
	s_cmp_ge_i32 s19, s16
	s_cselect_b64 s[12:13], -1, 0
	s_and_b64 s[14:15], s[12:13], exec
	s_cselect_b32 s14, s18, s16
	v_bfe_u32 v109, v104, 4, 2
	s_add_i32 s18, s14, s19
	s_bfe_i32 s28, s2, 0x10000
	s_and_b32 s14, s2, 1
	v_and_b32_e32 v113, 15, v104
	v_writelane_b32 v242, s8, 41
	v_lshlrev_b32_e32 v118, 2, v109
	s_bitcmp1_b32 s2, 0
	v_or_b32_e32 v147, s17, v113
	v_sub_u32_e32 v244, v147, v118
	v_subrev_u32_e32 v245, 64, v244
	v_writelane_b32 v242, s9, 42
	v_or_b32_e32 v8, s17, v118
	s_cselect_b64 s[16:17], -1, 0
	s_cmp_eq_u32 s14, 0
	v_writelane_b32 v242, s16, 31
	s_cselect_b64 s[14:15], -1, 0
	s_mul_hi_i32 s20, s18, 0x30c30c31
	v_writelane_b32 v242, s17, 32
	s_and_b64 s[16:17], s[14:15], exec
	s_mov_b32 s21, 0xc600000
	s_mov_b32 s16, 0xb800000
	s_cselect_b32 s30, s21, 0x8000000
	s_cselect_b32 s54, s16, 0x1000000
	s_or_b64 s[12:13], s[14:15], s[12:13]
	s_lshr_b32 s14, s20, 31
	s_ashr_i32 s34, s20, 10
	s_add_i32 s34, s34, s14
	s_mul_i32 s14, s34, 0xffffeb00
	s_add_i32 s41, s14, s18
	s_and_b64 s[14:15], s[12:13], exec
	s_cselect_b32 s35, s21, 0x8000000
	s_lshl_b32 s14, s41, 1
	s_add_i32 s14, s14, 0x7fffe400
	s_and_b32 s36, s14, 0x7fffffc0
	s_lshl_b32 s14, s19, 5
	s_and_b32 s37, s14, 0x3e0
	s_mul_hi_i32 s17, s41, 0x92492493
	s_and_b64 s[12:13], s[12:13], exec
	s_cselect_b32 s38, s16, 0x1000000
	s_add_i32 s17, s17, s41
	s_lshr_b32 s12, s17, 31
	s_ashr_i32 s13, s17, 7
	s_add_i32 s12, s13, s12
	s_mul_i32 s13, s12, 0xe0
	s_lshl_b32 s39, s12, 6
	s_sub_i32 s12, s41, s13
	s_lshl_b32 s40, s12, 5
	s_cmp_gt_i32 s26, -1
	s_cselect_b64 s[82:83], -1, 0
	s_cmp_gt_i32 s26, 0
	s_cselect_b64 s[12:13], -1, 0
	s_cmp_gt_i32 s26, 1
	s_cselect_b64 s[14:15], -1, 0
	s_cmp_gt_i32 s26, 2
	s_cselect_b64 s[16:17], -1, 0
	s_cmp_gt_i32 s26, 3
	s_cselect_b64 s[18:19], -1, 0
	s_cmp_gt_i32 s26, 4
	s_cselect_b64 s[20:21], -1, 0
	s_cmp_gt_i32 s26, 5
	s_cselect_b64 s[22:23], -1, 0
	s_cmp_gt_i32 s26, 6
	s_cselect_b64 s[24:25], -1, 0
	s_and_b64 s[42:43], s[6:7], s[42:43]
	v_writelane_b32 v242, s42, 43
	v_lshl_add_u32 v12, v8, 1, 0
	v_or_b32_e32 v8, 2, v118
	v_writelane_b32 v242, s43, 44
	v_cmp_gt_i32_e64 s[42:43], v118, v147
	v_bfe_u32 v5, v104, 2, 2
	v_lshlrev_b32_e32 v112, 3, v109
	v_writelane_b32 v243, s42, 31
	v_lshlrev_b32_e32 v7, 2, v107
	v_add_u32_e32 v149, s27, v7
	v_writelane_b32 v243, s43, 32
	v_cmp_lt_i32_e64 s[42:43], v118, v147
	v_add_u32_e32 v151, 0, v7
	v_and_b32_e32 v159, 28, v7
	v_writelane_b32 v243, s42, 33
	v_or_b32_e32 v7, v112, v5
	v_or_b32_e32 v5, v118, v5
	v_writelane_b32 v243, s43, 34
	v_cmp_gt_i32_e64 s[42:43], v8, v147
	v_or_b32_e32 v8, 3, v118
	s_cmpk_lt_i32 s41, 0xe00
	v_writelane_b32 v243, s42, 35
	v_mad_u32_u24 v160, v5, s3, v3
	v_mul_u32_u24_e32 v5, 0x110, v7
	v_writelane_b32 v243, s43, 36
	v_cmp_gt_i32_e64 s[42:43], v8, v147
	v_or_b32_e32 v8, 16, v118
	v_add3_u32 v164, s29, v108, v5
	v_writelane_b32 v243, s42, 37
	s_cselect_b32 s29, s40, s37
	s_mov_b32 s37, 0xe00000
	v_writelane_b32 v243, s43, 38
	v_cmp_gt_i32_e64 s[42:43], v8, v147
	v_or_b32_e32 v8, 17, v118
	v_mad_u32_u24 v165, v7, s3, v3
	v_writelane_b32 v243, s42, 39
	s_movk_i32 s3, 0x400
	s_cselect_b32 s35, s38, s35
	v_writelane_b32 v243, s43, 40
	v_cmp_gt_i32_e64 s[42:43], v8, v147
	v_or_b32_e32 v8, 18, v118
	s_cselect_b32 s37, s37, 0x700000
	v_writelane_b32 v243, s42, 41
	s_cselect_b32 s3, s3, 0xe00
	s_cselect_b32 s36, s39, s36
	v_writelane_b32 v243, s43, 42
	v_cmp_gt_i32_e64 s[42:43], v8, v147
	v_or_b32_e32 v8, 19, v118
	s_mul_hi_i32 s38, s37, s34
	v_writelane_b32 v243, s42, 43
	s_mul_i32 s37, s37, s34
	s_add_u32 s34, s51, s35
	v_writelane_b32 v243, s43, 44
	v_cmp_gt_i32_e64 s[42:43], v8, v147
	v_or_b32_e32 v8, 32, v118
	s_addc_u32 s35, s52, 0
	v_writelane_b32 v243, s42, 45
	s_add_u32 s39, s34, s37
	s_addc_u32 s38, s35, s38
	v_writelane_b32 v243, s43, 46
	v_cmp_gt_i32_e64 s[42:43], v8, v147
	v_or_b32_e32 v8, 33, v118
	s_ashr_i32 s37, s36, 31
	v_writelane_b32 v243, s42, 47
	s_lshl_b64 s[34:35], s[36:37], 1
	v_mov_b32_e32 v111, 0
	v_writelane_b32 v243, s43, 48
	v_cmp_gt_i32_e64 s[42:43], v8, v147
	v_or_b32_e32 v8, 34, v118
	v_and_b32_e32 v110, 48, v104
	v_writelane_b32 v243, s42, 49
	s_add_u32 s34, s39, s34
	v_lshlrev_b32_e32 v4, 3, v1
	v_writelane_b32 v243, s43, 50
	v_cmp_gt_i32_e64 s[42:43], v8, v147
	v_or_b32_e32 v8, 35, v118
	v_or_b32_e32 v156, 8, v154
	v_writelane_b32 v243, s42, 51
	v_lshl_add_u64 v[116:117], s[46:47], 0, v[110:111]
	v_add_u32_e32 v6, 0, v110
	v_writelane_b32 v243, s43, 52
	v_cmp_gt_i32_e64 s[42:43], v8, v147
	v_or_b32_e32 v8, 48, v118
	s_addc_u32 s35, s38, s35
	v_writelane_b32 v243, s42, 53
	v_lshlrev_b32_e32 v110, 4, v1
	v_or_b32_e32 v1, s29, v154
	v_writelane_b32 v243, s43, 54
	v_cmp_gt_i32_e64 s[42:43], v8, v147
	v_or_b32_e32 v8, 49, v118
	v_or_b32_e32 v157, 16, v154
	v_writelane_b32 v243, s42, 55
	v_or_b32_e32 v158, 24, v154
	s_lshr_b32 s2, s2, 1
	v_writelane_b32 v243, s43, 56
	v_cmp_gt_i32_e64 s[42:43], v8, v147
	v_or_b32_e32 v8, 50, v118
	v_lshlrev_b32_e32 v172, 2, v104
	v_writelane_b32 v243, s42, 57
	v_add_u32_e32 v3, 0, v172
	v_add_u32_e32 v3, 0x12b00, v3
	v_writelane_b32 v243, s43, 58
	v_cmp_gt_i32_e64 s[42:43], v8, v147
	v_or_b32_e32 v8, 51, v118
	s_lshl_b32 s41, s44, 4
	v_writelane_b32 v243, s42, 59
	v_and_b32_e32 v13, 0x7f, v104
	v_mul_u32_u24_e32 v14, 0x110, v113
	v_writelane_b32 v243, s43, 60
	v_cmp_gt_i32_e64 s[42:43], v8, v147
	v_or_b32_e32 v8, 64, v118
	v_or_b32_e32 v128, 0xffffff00, v13
	v_writelane_b32 v243, s42, 61
	v_mov_b32_e32 v115, v111
	v_mbcnt_hi_u32_b32 v180, -1, v212
	v_writelane_b32 v243, s43, 62
	v_cmp_gt_i32_e64 s[42:43], v8, v147
	v_or_b32_e32 v8, 0x41, v118
	s_movk_i32 s49, 0x100
	v_writelane_b32 v243, s42, 63
	v_writelane_b32 v243, s30, 14
	s_mov_b32 s55, s31
	v_writelane_b32 v242, s43, 0
	v_cmp_gt_i32_e64 s[42:43], v8, v147
	v_or_b32_e32 v8, 0x42, v118
	v_writelane_b32 v243, s31, 15
	v_writelane_b32 v242, s42, 1
	v_writelane_b32 v243, s44, 29
	v_sub_u32_e32 v129, 0xff, v119
	v_writelane_b32 v242, s43, 2
	v_cmp_gt_i32_e64 s[42:43], v8, v147
	v_or_b32_e32 v8, 0x43, v118
	v_sub_u32_e32 v148, 0xff, v147
	v_writelane_b32 v242, s42, 3
	v_add_u32_e32 v150, 0x100, v149
	v_cmp_lt_u32_e64 s[8:9], 15, v107
	v_writelane_b32 v242, s43, 4
	v_cmp_gt_i32_e64 s[42:43], v8, v147
	v_or_b32_e32 v8, 0x50, v118
	v_cmp_eq_u32_e64 s[10:11], 0, v107
	v_writelane_b32 v242, s42, 5
	v_add_u32_e32 v153, 0xffffff00, v147
	v_add_u32_e32 v161, 0xe00, v160
	v_writelane_b32 v242, s43, 6
	v_cmp_gt_i32_e64 s[42:43], v8, v147
	v_or_b32_e32 v8, 0x51, v118
	v_cmp_gt_i32_e64 s[56:57], v8, v147
	v_or_b32_e32 v8, 0x52, v118
	v_cmp_gt_i32_e64 s[58:59], v8, v147
	v_or_b32_e32 v8, 0x53, v118
	v_cmp_gt_i32_e64 s[60:61], v8, v147
	v_or_b32_e32 v8, 0x60, v118
	v_cmp_gt_i32_e64 s[62:63], v8, v147
	v_or_b32_e32 v8, 0x61, v118
	v_cmp_gt_i32_e64 s[64:65], v8, v147
	v_or_b32_e32 v8, 0x62, v118
	v_cmp_gt_i32_e64 s[66:67], v8, v147
	v_or_b32_e32 v8, 0x63, v118
	v_cmp_gt_i32_e64 s[68:69], v8, v147
	v_or_b32_e32 v8, 0x70, v118
	v_cmp_gt_i32_e64 s[70:71], v8, v147
	v_or_b32_e32 v8, 0x71, v118
	v_cmp_gt_i32_e64 s[72:73], v8, v147
	v_or_b32_e32 v8, 0x72, v118
	v_cmp_gt_i32_e64 s[74:75], v8, v147
	v_or_b32_e32 v8, 0x73, v118
	v_writelane_b32 v242, s42, 11
	v_cmp_gt_i32_e64 s[76:77], v8, v147
	v_lshl_add_u64 v[8:9], s[34:35], 0, v[110:111]
	v_mad_i64_i32 v[10:11], s[34:35], s3, v1, 0
	v_or_b32_e32 v1, s29, v156
	v_writelane_b32 v242, s43, 12
	v_lshl_add_u64 v[120:121], v[10:11], 1, v[8:9]
	v_mad_i64_i32 v[10:11], s[34:35], s3, v1, 0
	v_or_b32_e32 v1, s29, v157
	v_writelane_b32 v242, s51, 9
	v_lshl_add_u64 v[122:123], v[10:11], 1, v[8:9]
	v_mad_i64_i32 v[10:11], s[34:35], s3, v1, 0
	v_or_b32_e32 v1, s29, v158
	v_writelane_b32 v242, s52, 30
	v_lshl_add_u64 v[124:125], v[10:11], 1, v[8:9]
	v_mad_i64_i32 v[10:11], s[34:35], s3, v1, 0
	s_lshl_b32 s3, s45, 5
	v_max_i32_e32 v1, 0x700, v104
	v_writelane_b32 v242, s45, 19
	s_and_b32 s3, s3, 0x3e0
	v_sub_u32_e32 v1, v1, v104
	v_writelane_b32 v242, s3, 36
	v_add_u32_e32 v1, 0x1ff, v1
	v_writelane_b32 v242, s54, 39
	s_and_b32 s3, s28, 3
	v_lshrrev_b32_e32 v5, 9, v1
	v_writelane_b32 v242, s55, 40
	s_lshl_b32 s2, s2, s3
	v_add_u32_e32 v7, 1, v5
	v_add_u32_e32 v5, -1, v5
	v_lshl_add_u64 v[126:127], v[10:11], 1, v[8:9]
	v_writelane_b32 v242, s2, 33
	v_lshlrev_b32_e32 v9, 2, v1
	v_cmp_lt_u32_e64 s[28:29], 1, v5
	v_lshrrev_b32_e32 v8, 1, v5
	s_movk_i32 s2, 0xdff
	v_and_b32_e32 v9, 0xfffff800, v9
	v_writelane_b32 v242, s28, 53
	v_and_b32_e32 v5, 2, v5
	v_cmp_lt_u32_e32 vcc, s2, v1
	v_cmp_gt_u32_e64 s[2:3], 2.0, v1
	v_add_u32_e32 v1, v3, v9
	v_writelane_b32 v242, s29, 54
	v_cmp_eq_u32_e64 s[28:29], 0, v5
	v_cmp_ge_u32_e64 s[78:79], v1, v3
	v_and_b32_e32 v3, 0xfffffe, v7
	v_writelane_b32 v242, s28, 55
	s_and_b64 s[2:3], s[78:79], s[2:3]
	s_and_b64 s[2:3], vcc, s[2:3]
	v_writelane_b32 v242, s29, 56
	v_cmp_ne_u32_e64 s[28:29], v7, v3
	v_lshl_add_u32 v173, v3, 9, v104
	v_lshl_add_u32 v3, v104, 4, 0
	v_writelane_b32 v242, s28, 57
	v_add_u32_e32 v8, 1, v8
	v_add_u32_e32 v175, 0xc000, v3
	v_writelane_b32 v242, s29, 58
	v_writelane_b32 v242, s2, 49
	v_bfrev_b32_e32 v7, 0.5
	v_add_u32_e32 v162, 0x1c00, v160
	v_writelane_b32 v242, s3, 50
	v_writelane_b32 v242, s46, 25
	s_sub_i32 s2, 0, s41
	s_lshl_b32 s3, s26, 1
	v_writelane_b32 v242, s47, 26
	v_writelane_b32 v242, s2, 23
	s_lshl_b32 s2, s50, 4
	s_add_i32 s2, s2, s3
	s_add_i32 s2, s2, 0x80007400
	v_writelane_b32 v242, s2, 51
	s_add_i32 s2, 0, 0x25de0
	v_writelane_b32 v242, s2, 21
	s_add_i32 s2, 0, 0x25db8
	v_writelane_b32 v243, s2, 19
	s_add_i32 s2, 0, 0x25dd0
	v_writelane_b32 v243, s2, 20
	s_add_i32 s2, 0, 0x25da8
	v_writelane_b32 v242, s2, 10
	s_add_i32 s2, 0, 0x25dd8
	v_writelane_b32 v243, s2, 21
	s_add_i32 s2, 0, 0x25db0
	v_writelane_b32 v243, s2, 23
	s_add_i32 s2, s48, 0x820
	v_writelane_b32 v242, s2, 34
	s_add_i32 s2, s48, 0xc30
	v_writelane_b32 v242, s2, 35
	s_add_i32 s2, s48, 0x1040
	v_writelane_b32 v242, s2, 38
	s_add_i32 s2, s48, 0x1450
	v_writelane_b32 v242, s2, 24
	s_add_i32 s2, s48, 0x1860
	v_writelane_b32 v242, s2, 27
	v_add_u32_e32 v163, 0x2a00, v160
	v_add_u32_e32 v166, 0x2200, v164
	v_add_u32_e32 v167, 0xe00, v165
	v_add_u32_e32 v168, 0x4400, v164
	v_add_u32_e32 v169, 0x1c00, v165
	v_add_u32_e32 v170, 0x6600, v164
	v_add_u32_e32 v171, 0x2a00, v165
	v_mov_b32_e32 v1, v128
	v_add_u32_e32 v105, 0x200, v104
	v_and_b32_e32 v174, -2, v8
	v_lshl_add_u64 v[130:131], s[46:47], 0, v[114:115]
	v_add_u32_e32 v115, 0xfffffe00, v104
	v_add_u32_e32 v176, s27, v172
	s_sub_i32 s40, 0, s33
	v_add_u32_e32 v177, 0x10900, v151
	v_sub_u32_e32 v178, 0, v119
	v_lshlrev_b32_e32 v132, 1, v112
	s_mov_b32 s42, 0x3f2aaaab
	v_mov_b32_e32 v179, 0x3ecc95a3
	s_mov_b32 s43, 0x3f317218
	s_mov_b32 s44, 0x7f800000
	s_mov_b32 s45, 0x33800000
	v_lshlrev_b32_e32 v134, 2, v118
	v_add_u32_e32 v181, v2, v114
	s_xor_b64 s[26:27], s[6:7], -1
	v_lshlrev_b32_e32 v110, 1, v4
	v_writelane_b32 v242, s48, 7
	s_add_i32 s2, s48, 0x1c70
	v_add_u32_e32 v182, v12, v14
	v_mov_b32_e32 v2, v111
	v_mov_b32_e32 v3, v111
	v_mov_b32_e32 v4, v111
	v_mov_b32_e32 v5, v111
	v_mov_b32_e32 v136, 0x3f317218
	v_mov_b32_e32 v183, 0x7f800000
	v_mov_b32_e32 v184, 0x7fc00000
	v_mov_b32_e32 v185, 0xff800000
	v_lshl_or_b32 v186, v180, 2, v7
	v_add_u32_e32 v187, v6, v14
	v_mov_b32_e32 v188, 0x7c
	v_writelane_b32 v242, s2, 29
	s_branch .LBB0_4992

.LBB0_5096:
	v_lshl_add_u32 v137, v147, 2, s81
	ds_read_b32 v139, v137 offset:62720
	v_lshl_add_u32 v192, v118, 2, s81
	s_mov_b64 s[36:37], -1
	s_and_b64 vcc, exec, s[82:83]
	s_cbranch_vccz .LBB0_5113
	ds_read_b128 v[194:197], v192 offset:62208
	v_cmp_gt_i32_e64 s[36:37], 0, v244
	s_waitcnt lgkmcnt(0)
	v_sub_f32_e32 v70, v194, v139
	v_sub_f32_e32 v71, v195, v139
	v_mul_f32_e32 v70, 0x3fb8aa3b, v70
	v_mul_f32_e32 v71, 0x3fb8aa3b, v71
	v_exp_f32_e32 v70, v70
	v_exp_f32_e32 v71, v71
	v_sub_f32_e32 v193, v196, v139
	v_mul_f32_e32 v193, 0x3fb8aa3b, v193
	v_fma_mixlo_f16 v70, v100, v70, 0
	v_fma_mixlo_f16 v71, v101, v71, 0
	v_exp_f32_e32 v100, v193
	v_sub_f32_e32 v101, v197, v139
	v_cndmask_b32_e64 v70, v70, 0, s[36:37]
	v_readlane_b32 s36, v243, 33
	v_mul_f32_e32 v101, 0x3fb8aa3b, v101
	v_readlane_b32 s37, v243, 34
	v_exp_f32_e32 v101, v101
	s_nop 0
	v_cndmask_b32_e64 v71, 0, v71, s[36:37]
	v_pack_b32_f16 v70, v70, v71
	v_fma_mixlo_f16 v71, v102, v100, 0
	v_cmp_gt_i32_e64 s[36:37], 2, v244
	v_fma_mixlo_f16 v100, v103, v101, 0
	s_nop 0
	v_cndmask_b32_e64 v71, v71, 0, s[36:37]
	v_cmp_gt_i32_e64 s[36:37], 3, v244
	s_nop 1
	v_cndmask_b32_e64 v100, v100, 0, s[36:37]
	v_pack_b32_f16 v71, v71, v100
	s_cbranch_execz .LBB0_5114

.LBB0_5099:
	ds_read_b128 v[100:103], v192 offset:62272
	v_cmp_gt_i32_e64 s[36:37], 16, v244
	s_waitcnt lgkmcnt(0)
	v_sub_f32_e32 v100, v100, v139
	v_sub_f32_e32 v101, v101, v139
	v_mul_f32_e32 v100, 0x3fb8aa3b, v100
	v_mul_f32_e32 v101, 0x3fb8aa3b, v101
	v_exp_f32_e32 v100, v100
	v_exp_f32_e32 v101, v101
	v_sub_f32_e32 v102, v102, v139
	v_mul_f32_e32 v102, 0x3fb8aa3b, v102
	v_fma_mixlo_f16 v72, v72, v100, 0
	v_fma_mixlo_f16 v73, v73, v101, 0
	v_exp_f32_e32 v100, v102
	v_sub_f32_e32 v101, v103, v139
	v_cndmask_b32_e64 v72, v72, 0, s[36:37]
	v_mul_f32_e32 v101, 0x3fb8aa3b, v101
	v_cmp_gt_i32_e64 s[36:37], 17, v244
	v_exp_f32_e32 v101, v101
	s_nop 0
	v_cndmask_b32_e64 v73, v73, 0, s[36:37]
	v_pack_b32_f16 v72, v72, v73
	v_fma_mixlo_f16 v73, v74, v100, 0
	v_cmp_gt_i32_e64 s[36:37], 18, v244
	v_fma_mixlo_f16 v74, v75, v101, 0
	s_nop 0
	v_cndmask_b32_e64 v73, v73, 0, s[36:37]
	v_cmp_gt_i32_e64 s[36:37], 19, v244
	s_nop 1
	v_cndmask_b32_e64 v74, v74, 0, s[36:37]
	v_pack_b32_f16 v73, v73, v74
	s_cbranch_execz .LBB0_5116

.LBB0_5101:
	ds_read_b128 v[100:103], v192 offset:62336
	v_cmp_gt_i32_e64 s[36:37], 32, v244
	s_waitcnt lgkmcnt(0)
	v_sub_f32_e32 v74, v100, v139
	v_sub_f32_e32 v75, v101, v139
	v_mul_f32_e32 v74, 0x3fb8aa3b, v74
	v_mul_f32_e32 v75, 0x3fb8aa3b, v75
	v_exp_f32_e32 v74, v74
	v_exp_f32_e32 v75, v75
	v_sub_f32_e32 v100, v102, v139
	v_mul_f32_e32 v100, 0x3fb8aa3b, v100
	v_fma_mixlo_f16 v74, v96, v74, 0
	v_fma_mixlo_f16 v75, v97, v75, 0
	v_exp_f32_e32 v96, v100
	v_sub_f32_e32 v97, v103, v139
	v_cndmask_b32_e64 v74, v74, 0, s[36:37]
	v_mul_f32_e32 v97, 0x3fb8aa3b, v97
	v_cmp_gt_i32_e64 s[36:37], 33, v244
	v_exp_f32_e32 v97, v97
	s_nop 0
	v_cndmask_b32_e64 v75, v75, 0, s[36:37]
	v_pack_b32_f16 v74, v74, v75
	v_fma_mixlo_f16 v75, v98, v96, 0
	v_cmp_gt_i32_e64 s[36:37], 34, v244
	v_fma_mixlo_f16 v96, v99, v97, 0
	s_nop 0
	v_cndmask_b32_e64 v75, v75, 0, s[36:37]
	v_cmp_gt_i32_e64 s[36:37], 35, v244
	s_nop 1
	v_cndmask_b32_e64 v96, v96, 0, s[36:37]
	v_pack_b32_f16 v75, v75, v96
	s_cbranch_execz .LBB0_5118

.LBB0_5103:
	ds_read_b128 v[96:99], v192 offset:62400
	v_cmp_gt_i32_e64 s[2:3], 48, v244
	s_waitcnt lgkmcnt(0)
	v_sub_f32_e32 v96, v96, v139
	v_sub_f32_e32 v97, v97, v139
	v_mul_f32_e32 v96, 0x3fb8aa3b, v96
	v_mul_f32_e32 v97, 0x3fb8aa3b, v97
	v_exp_f32_e32 v96, v96
	v_exp_f32_e32 v97, v97
	v_sub_f32_e32 v98, v98, v139
	v_mul_f32_e32 v98, 0x3fb8aa3b, v98
	v_fma_mixlo_f16 v76, v76, v96, 0
	v_fma_mixlo_f16 v77, v77, v97, 0
	v_exp_f32_e32 v96, v98
	v_sub_f32_e32 v97, v99, v139
	v_cndmask_b32_e64 v76, v76, 0, s[2:3]
	v_mul_f32_e32 v97, 0x3fb8aa3b, v97
	v_cmp_gt_i32_e64 s[2:3], 49, v244
	v_exp_f32_e32 v97, v97
	s_nop 0
	v_cndmask_b32_e64 v77, v77, 0, s[2:3]
	v_pack_b32_f16 v76, v76, v77
	v_fma_mixlo_f16 v77, v78, v96, 0
	v_cmp_gt_i32_e64 s[2:3], 50, v244
	v_fma_mixlo_f16 v78, v79, v97, 0
	s_nop 0
	v_cndmask_b32_e64 v77, v77, 0, s[2:3]
	v_cmp_gt_i32_e64 s[2:3], 51, v244
	s_nop 1
	v_cndmask_b32_e64 v78, v78, 0, s[2:3]
	v_pack_b32_f16 v77, v77, v78
	s_cbranch_execz .LBB0_5120

.LBB0_5105:
	ds_read_b128 v[96:99], v192 offset:62464
	v_cmp_gt_i32_e64 s[2:3], 0, v245
	s_waitcnt lgkmcnt(0)
	v_sub_f32_e32 v78, v96, v139
	v_sub_f32_e32 v79, v97, v139
	v_mul_f32_e32 v78, 0x3fb8aa3b, v78
	v_mul_f32_e32 v79, 0x3fb8aa3b, v79
	v_exp_f32_e32 v78, v78
	v_exp_f32_e32 v79, v79
	v_sub_f32_e32 v96, v98, v139
	v_mul_f32_e32 v96, 0x3fb8aa3b, v96
	v_fma_mixlo_f16 v78, v92, v78, 0
	v_fma_mixlo_f16 v79, v93, v79, 0
	v_exp_f32_e32 v92, v96
	v_sub_f32_e32 v93, v99, v139
	v_cndmask_b32_e64 v78, v78, 0, s[2:3]
	v_mul_f32_e32 v93, 0x3fb8aa3b, v93
	v_cmp_gt_i32_e64 s[2:3], 1, v245
	v_exp_f32_e32 v93, v93
	s_nop 0
	v_cndmask_b32_e64 v79, v79, 0, s[2:3]
	v_pack_b32_f16 v78, v78, v79
	v_fma_mixlo_f16 v79, v94, v92, 0
	v_cmp_gt_i32_e64 s[2:3], 2, v245
	v_fma_mixlo_f16 v92, v95, v93, 0
	s_nop 0
	v_cndmask_b32_e64 v79, v79, 0, s[2:3]
	v_cmp_gt_i32_e64 s[2:3], 3, v245
	s_nop 1
	v_cndmask_b32_e64 v92, v92, 0, s[2:3]
	v_pack_b32_f16 v79, v79, v92
	s_cbranch_execz .LBB0_5122

.LBB0_5107:
	ds_read_b128 v[92:95], v192 offset:62528
	v_cmp_gt_i32_e64 s[2:3], 16, v245
	s_waitcnt lgkmcnt(0)
	v_sub_f32_e32 v93, v93, v139
	v_mul_f32_e32 v93, 0x3fb8aa3b, v93
	v_sub_f32_e32 v92, v92, v139
	v_exp_f32_e32 v93, v93
	v_mul_f32_e32 v92, 0x3fb8aa3b, v92
	v_exp_f32_e32 v92, v92
	v_sub_f32_e32 v94, v94, v139
	v_fma_mixlo_f16 v81, v81, v93, 0
	v_sub_f32_e32 v93, v95, v139
	v_mul_f32_e32 v94, 0x3fb8aa3b, v94
	v_mul_f32_e32 v93, 0x3fb8aa3b, v93
	v_fma_mixlo_f16 v80, v80, v92, 0
	v_exp_f32_e32 v92, v94
	v_exp_f32_e32 v93, v93
	v_cndmask_b32_e64 v80, v80, 0, s[2:3]
	v_cndmask_b32_e64 v81, v81, 0, s[56:57]
	v_pack_b32_f16 v80, v80, v81
	v_fma_mixlo_f16 v81, v82, v92, 0
	v_fma_mixlo_f16 v82, v83, v93, 0
	v_cndmask_b32_e64 v81, v81, 0, s[58:59]
	v_cndmask_b32_e64 v82, v82, 0, s[60:61]
	v_pack_b32_f16 v81, v81, v82
	s_cbranch_execz .LBB0_5124

	.amdhsa_kernel _Z4mega4Args
		.amdhsa_group_segment_fixed_size 0
		.amdhsa_private_segment_fixed_size 0
		.amdhsa_kernarg_size 512
		.amdhsa_user_sgpr_count 2
		.amdhsa_user_sgpr_dispatch_ptr 0
		.amdhsa_user_sgpr_queue_ptr 0
		.amdhsa_user_sgpr_kernarg_segment_ptr 1
		.amdhsa_user_sgpr_dispatch_id 0
		.amdhsa_user_sgpr_kernarg_preload_length 0
		.amdhsa_user_sgpr_kernarg_preload_offset 0
		.amdhsa_user_sgpr_private_segment_size 0
		.amdhsa_uses_dynamic_stack 0
		.amdhsa_enable_private_segment 0
		.amdhsa_system_sgpr_workgroup_id_x 1
		.amdhsa_system_sgpr_workgroup_id_y 0
		.amdhsa_system_sgpr_workgroup_id_z 0
		.amdhsa_system_sgpr_workgroup_info 0
		.amdhsa_system_vgpr_workitem_id 0
		.amdhsa_next_free_vgpr 248
		.amdhsa_next_free_sgpr 102
		.amdhsa_accum_offset 248
		.amdhsa_reserve_vcc 1
		.amdhsa_float_round_mode_32 0
		.amdhsa_float_round_mode_16_64 0
		.amdhsa_float_denorm_mode_32 3
		.amdhsa_float_denorm_mode_16_64 3
		.amdhsa_dx10_clamp 1
		.amdhsa_ieee_mode 1
		.amdhsa_fp16_overflow 0
		.amdhsa_tg_split 0
		.amdhsa_exception_fp_ieee_invalid_op 0
		.amdhsa_exception_fp_denorm_src 0
		.amdhsa_exception_fp_ieee_div_zero 0
		.amdhsa_exception_fp_ieee_overflow 0
		.amdhsa_exception_fp_ieee_underflow 0
		.amdhsa_exception_fp_ieee_inexact 0
		.amdhsa_exception_int_div_zero 0
	.end_amdhsa_kernel

amdhsa.kernels:
  - .agpr_count:     0
    .args:
      - .offset:         0
        .size:           256
        .value_kind:     by_value
      - .offset:         256
        .size:           4
        .value_kind:     hidden_block_count_x
      - .offset:         260
        .size:           4
        .value_kind:     hidden_block_count_y
      - .offset:         264
        .size:           4
        .value_kind:     hidden_block_count_z
      - .offset:         268
        .size:           2
        .value_kind:     hidden_group_size_x
      - .offset:         270
        .size:           2
        .value_kind:     hidden_group_size_y
      - .offset:         272
        .size:           2
        .value_kind:     hidden_group_size_z
      - .offset:         274
        .size:           2
        .value_kind:     hidden_remainder_x
      - .offset:         276
        .size:           2
        .value_kind:     hidden_remainder_y
      - .offset:         278
        .size:           2
        .value_kind:     hidden_remainder_z
      - .offset:         296
        .size:           8
        .value_kind:     hidden_global_offset_x
      - .offset:         304
        .size:           8
        .value_kind:     hidden_global_offset_y
      - .offset:         312
        .size:           8
        .value_kind:     hidden_global_offset_z
      - .offset:         320
        .size:           2
        .value_kind:     hidden_grid_dims
      - .offset:         376
        .size:           4
        .value_kind:     hidden_dynamic_lds_size
    .group_segment_fixed_size: 0
    .kernarg_segment_align: 8
    .kernarg_segment_size: 512
    .language:       OpenCL C
    .language_version:
      - 2
      - 0
    .max_flat_workgroup_size: 512
    .name:           _Z4mega4Args
    .private_segment_fixed_size: 0
    .sgpr_count:     108
    .sgpr_spill_count: 386
    .symbol:         _Z4mega4Args.kd
    .uniform_work_group_size: 1
    .uses_dynamic_stack: false
    .vgpr_count:     248
    .vgpr_spill_count: 0
    .wavefront_size: 64
